# speedup vs baseline: 1.0053x; 1.0053x over previous
.LBB3_33:
	s_or_b64 exec, exec, s[4:5]
	s_add_u32 s4, s20, 0x100000
	s_mul_hi_u32 s2, s26, 0xaaaaaaab
	s_addc_u32 s5, s21, 0
	s_lshr_b32 s6, s2, 8
	s_mul_hi_u32 s2, s27, 0x2aaaaaab
	s_mul_i32 s2, s2, 6
	s_sub_i32 s2, s27, s2
	s_waitcnt vmcnt(5)
	v_mov_b32_e32 v2, s2
	v_sub_co_u32_e64 v3, s[2:3], s2, 3
	v_mov_b32_e32 v85, 0
	s_nop 0
	v_cndmask_b32_e64 v2, v3, v2, s[2:3]
	s_and_b64 s[2:3], s[2:3], exec
	s_cselect_b32 s2, s28, s29
	s_mul_i32 s2, s2, 49
	s_add_i32 s2, s2, s6
	s_mul_hi_u32 s3, s2, 3
	s_mul_i32 s2, s2, 3
	v_mov_b32_e32 v3, v85
	v_lshl_add_u64 v[2:3], s[2:3], 0, v[2:3]
	s_add_i32 s2, s27, 4
	s_mul_hi_u32 s6, s2, 0x2aaaaaab
	v_lshlrev_b64 v[2:3], 10, v[2:3]
	s_mul_i32 s3, s6, 6
	v_lshlrev_b32_e32 v84, 4, v92
	v_lshl_add_u64 v[2:3], s[4:5], 0, v[2:3]
	s_sub_i32 s2, s2, s3
	v_lshl_add_u64 v[86:87], v[2:3], 0, v[84:85]
	v_mov_b32_e32 v2, s2
	v_sub_co_u32_e64 v3, s[2:3], s2, 3
	s_nop 1
	v_cndmask_b32_e64 v2, v3, v2, s[2:3]
	s_and_b64 s[2:3], s[2:3], exec
	s_cselect_b32 s2, s28, s29
	s_mul_i32 s2, s2, 49
	s_add_i32 s2, s2, s6
	s_mul_hi_u32 s3, s2, 3
	s_mul_i32 s2, s2, 3
	v_mov_b32_e32 v3, v85
	v_lshl_add_u64 v[2:3], s[2:3], 0, v[2:3]
	s_add_i32 s2, s27, 8
	s_mul_hi_u32 s6, s2, 0x2aaaaaab
	v_lshlrev_b64 v[2:3], 10, v[2:3]
	s_mul_i32 s3, s6, 6
	v_lshl_add_u64 v[2:3], s[4:5], 0, v[2:3]
	s_sub_i32 s2, s2, s3
	v_lshl_add_u64 v[88:89], v[2:3], 0, v[84:85]
	v_mov_b32_e32 v2, s2
	v_sub_co_u32_e64 v3, s[2:3], s2, 3
	s_nop 1
	v_cndmask_b32_e64 v2, v3, v2, s[2:3]
	s_and_b64 s[2:3], s[2:3], exec
	s_cselect_b32 s2, s28, s29
	s_mul_i32 s2, s2, 49
	s_add_i32 s2, s2, s6
	s_mul_hi_u32 s3, s2, 3
	s_mul_i32 s2, s2, 3
	v_mov_b32_e32 v3, v85
	v_lshl_add_u64 v[2:3], s[2:3], 0, v[2:3]
	v_lshlrev_b64 v[2:3], 10, v[2:3]
	v_lshl_add_u64 v[2:3], s[4:5], 0, v[2:3]
	s_and_b32 s2, s26, 0xfffffc0
	v_lshl_add_u64 v[90:91], v[2:3], 0, v[84:85]
	v_lshl_or_b32 v93, s2, 4, v84
	v_readfirstlane_b32 s40, v86
	v_readfirstlane_b32 s41, v87
	v_readfirstlane_b32 s42, v88
	v_readfirstlane_b32 s43, v89
	v_readfirstlane_b32 s44, v90
	v_readfirstlane_b32 s45, v91
	s_lshl_b32 s46, s27, 10
	s_add_u32 s47, s46, 0x1000
	s_add_u32 s48, s46, 0x2000
	s_movk_i32 s50, 0xc00
	s_movk_i32 s51, 0x1800
	s_cmp_ge_u32 s27, 2
	s_cselect_b32 s49, s50, s51
	v_and_b32_e32 v99, 31, v92
	v_mov_b32_e32 v79, 0x150
	v_cmp_gt_u32_e64 s[52:53], 21, v99
	s_cmp_eq_u32 s27, 2
	s_cselect_b64 s[54:55], -1, 0
	v_cndmask_b32_e64 v99, v79, v84, s[52:53]
	s_cmp_eq_u32 s27, 1
	s_cselect_b64 s[56:57], -1, 0
	s_or_b64 s[58:59], s[54:55], s[56:57]
	s_not_b64 s[58:59], s[58:59]
	v_cndmask_b32_e64 v76, v84, v99, s[54:55]
	v_cndmask_b32_e64 v77, v84, v99, s[56:57]
	v_cndmask_b32_e64 v78, v84, v99, s[58:59]
	s_waitcnt lgkmcnt(0)
	s_nop 4
	s_andn2_b64 vcc, exec, vcc
	s_mov_b64 s[2:3], -1
	s_cbranch_vccnz .LBB3_35
	s_add_u32 m0, s46, 0x0
	s_nop 0
	global_load_lds_dwordx4 v76, s[40:41]
	s_add_u32 m0, s47, 0x0
	s_nop 0
	global_load_lds_dwordx4 v77, s[42:43]
	s_add_u32 m0, s48, 0x0
	s_nop 0
	global_load_lds_dwordx4 v78, s[44:45]
	s_add_u32 m0, s46, 0x3000
	s_add_u32 s40, s40, 0x1800
	s_addc_u32 s41, s41, 0
	global_load_lds_dwordx4 v76, s[40:41]
	s_add_u32 m0, s47, 0x3000
	s_add_u32 s42, s42, 0x1800
	s_addc_u32 s43, s43, 0
	global_load_lds_dwordx4 v77, s[42:43]
	s_add_u32 m0, s48, 0x3000
	s_add_u32 s44, s44, 0x1800
	s_addc_u32 s45, s45, 0
	global_load_lds_dwordx4 v78, s[44:45]
	s_add_u32 m0, s46, 0xd3c0
	s_add_u32 s40, s40, 0x1800
	s_addc_u32 s41, s41, 0
	global_load_lds_dwordx4 v76, s[40:41]
	s_add_u32 m0, s47, 0xd3c0
	s_add_u32 s42, s42, 0x1800
	s_addc_u32 s43, s43, 0
	global_load_lds_dwordx4 v77, s[42:43]
	s_add_u32 m0, s48, 0xd3c0
	s_add_u32 s44, s44, 0x1800
	s_addc_u32 s45, s45, 0
	global_load_lds_dwordx4 v78, s[44:45]
	s_add_u32 m0, s46, 0x103c0
	s_add_u32 s40, s40, 0x1800
	s_addc_u32 s41, s41, 0
	global_load_lds_dwordx4 v76, s[40:41]
	s_add_u32 m0, s47, 0x103c0
	s_add_u32 s42, s42, 0x1800
	s_addc_u32 s43, s43, 0
	global_load_lds_dwordx4 v77, s[42:43]
	s_add_u32 m0, s48, 0x103c0
	s_add_u32 s44, s44, 0x1800
	s_addc_u32 s45, s45, 0
	global_load_lds_dwordx4 v78, s[44:45]
	s_waitcnt vmcnt(9)
	s_barrier
	s_waitcnt vmcnt(6)
	s_barrier
	s_add_u32 m0, s46, 0x0
	s_add_u32 s40, s40, 0x1800
	s_addc_u32 s41, s41, 0
	global_load_lds_dwordx4 v76, s[40:41]
	s_add_u32 m0, s47, 0x0
	s_add_u32 s42, s42, 0x1800
	s_addc_u32 s43, s43, 0
	global_load_lds_dwordx4 v77, s[42:43]
	s_add_u32 m0, s48, 0x0
	s_add_u32 s44, s44, 0x1800
	s_addc_u32 s45, s45, 0
	global_load_lds_dwordx4 v78, s[44:45]
	s_waitcnt vmcnt(6)
	s_barrier
	s_add_u32 m0, s46, 0x3000
	s_add_u32 s40, s40, 0x1800
	s_addc_u32 s41, s41, 0
	global_load_lds_dwordx4 v76, s[40:41]
	s_add_u32 m0, s47, 0x3000
	s_add_u32 s42, s42, 0x1800
	s_addc_u32 s43, s43, 0
	global_load_lds_dwordx4 v77, s[42:43]
	s_add_u32 m0, s48, 0x3000
	s_add_u32 s44, s44, 0x1800
	s_addc_u32 s45, s45, 0
	global_load_lds_dwordx4 v78, s[44:45]
	s_waitcnt vmcnt(6)
	s_barrier
	s_add_u32 m0, s46, 0xd3c0
	s_add_u32 s40, s40, 0x1800
	s_addc_u32 s41, s41, 0
	global_load_lds_dwordx4 v76, s[40:41]
	s_add_u32 m0, s47, 0xd3c0
	s_add_u32 s42, s42, 0x1800
	s_addc_u32 s43, s43, 0
	global_load_lds_dwordx4 v77, s[42:43]
	s_add_u32 m0, s48, 0xd3c0
	s_add_u32 s44, s44, 0x1800
	s_addc_u32 s45, s45, 0
	global_load_lds_dwordx4 v78, s[44:45]
	s_waitcnt vmcnt(6)
	s_barrier
	s_add_u32 m0, s46, 0x103c0
	s_add_u32 s40, s40, 0x1800
	s_addc_u32 s41, s41, 0
	global_load_lds_dwordx4 v76, s[40:41]
	s_add_u32 m0, s47, 0x103c0
	s_add_u32 s42, s42, 0x1800
	s_addc_u32 s43, s43, 0
	global_load_lds_dwordx4 v77, s[42:43]
	s_add_u32 m0, s48, 0x103c0
	s_add_u32 s44, s44, 0x1800
	s_addc_u32 s45, s45, 0
	global_load_lds_dwordx4 v78, s[44:45]
	s_waitcnt vmcnt(6)
	s_barrier
	s_add_u32 m0, s46, 0x0
	s_add_u32 s40, s40, 0x1800
	s_addc_u32 s41, s41, 0
	global_load_lds_dwordx4 v76, s[40:41]
	s_add_u32 m0, s47, 0x0
	s_add_u32 s42, s42, 0x1800
	s_addc_u32 s43, s43, 0
	global_load_lds_dwordx4 v77, s[42:43]
	s_add_u32 m0, s48, 0x0
	s_add_u32 s44, s44, 0x1800
	s_addc_u32 s45, s45, 0
	global_load_lds_dwordx4 v78, s[44:45]
	s_waitcnt vmcnt(6)
	s_barrier
	s_add_u32 m0, s46, 0x3000
	s_add_u32 s40, s40, 0x1800
	s_addc_u32 s41, s41, 0
	global_load_lds_dwordx4 v76, s[40:41]
	s_add_u32 m0, s47, 0x3000
	s_add_u32 s42, s42, 0x1800
	s_addc_u32 s43, s43, 0
	global_load_lds_dwordx4 v77, s[42:43]
	s_add_u32 m0, s48, 0x3000
	s_add_u32 s44, s44, 0x1800
	s_addc_u32 s45, s45, 0
	global_load_lds_dwordx4 v78, s[44:45]
	s_waitcnt vmcnt(6)
	s_barrier
	s_add_u32 m0, s46, 0xd3c0
	s_add_u32 s40, s40, 0x1800
	s_addc_u32 s41, s41, 0
	global_load_lds_dwordx4 v76, s[40:41]
	s_add_u32 m0, s47, 0xd3c0
	s_add_u32 s42, s42, 0x1800
	s_addc_u32 s43, s43, 0
	global_load_lds_dwordx4 v77, s[42:43]
	s_add_u32 m0, s48, 0xd3c0
	s_add_u32 s44, s44, 0x1800
	s_addc_u32 s45, s45, 0
	global_load_lds_dwordx4 v78, s[44:45]
	s_waitcnt vmcnt(6)
	s_barrier
	s_add_u32 m0, s46, 0x103c0
	s_add_u32 s40, s40, 0x1800
	s_addc_u32 s41, s41, 0
	global_load_lds_dwordx4 v76, s[40:41]
	s_add_u32 m0, s47, 0x103c0
	s_add_u32 s42, s42, 0x1800
	s_addc_u32 s43, s43, 0
	global_load_lds_dwordx4 v77, s[42:43]
	s_add_u32 m0, s48, 0x103c0
	s_add_u32 s44, s44, 0x1800
	s_addc_u32 s45, s45, 0
	global_load_lds_dwordx4 v78, s[44:45]
	s_waitcnt vmcnt(6)
	s_barrier
	s_add_u32 m0, s46, 0x0
	s_add_u32 s40, s40, 0x1800
	s_addc_u32 s41, s41, 0
	global_load_lds_dwordx4 v76, s[40:41]
	s_add_u32 m0, s47, 0x0
	s_add_u32 s42, s42, 0x1800
	s_addc_u32 s43, s43, 0
	global_load_lds_dwordx4 v77, s[42:43]
	s_add_u32 m0, s48, 0x0
	s_add_u32 s44, s44, 0x1800
	s_addc_u32 s45, s45, 0
	global_load_lds_dwordx4 v78, s[44:45]
	s_waitcnt vmcnt(6)
	s_barrier
	s_add_u32 m0, s46, 0x3000
	s_add_u32 s40, s40, 0x1800
	s_addc_u32 s41, s41, 0
	global_load_lds_dwordx4 v76, s[40:41]
	s_add_u32 m0, s47, 0x3000
	s_add_u32 s42, s42, 0x1800
	s_addc_u32 s43, s43, 0
	global_load_lds_dwordx4 v77, s[42:43]
	s_add_u32 m0, s48, 0x3000
	s_add_u32 s44, s44, 0x1800
	s_addc_u32 s45, s45, 0
	global_load_lds_dwordx4 v78, s[44:45]
	s_waitcnt vmcnt(6)
	s_barrier
	s_add_u32 m0, s46, 0xd3c0
	s_add_u32 s40, s40, 0x1800
	s_addc_u32 s41, s41, 0
	global_load_lds_dwordx4 v76, s[40:41]
	s_add_u32 m0, s47, 0xd3c0
	s_add_u32 s42, s42, 0x1800
	s_addc_u32 s43, s43, 0
	global_load_lds_dwordx4 v77, s[42:43]
	s_add_u32 m0, s48, 0xd3c0
	s_add_u32 s44, s44, 0x1800
	s_addc_u32 s45, s45, 0
	global_load_lds_dwordx4 v78, s[44:45]
	s_waitcnt vmcnt(6)
	s_barrier
	s_add_u32 m0, s46, 0x103c0
	s_add_u32 s40, s40, 0x1800
	s_addc_u32 s41, s41, 0
	global_load_lds_dwordx4 v76, s[40:41]
	s_add_u32 m0, s47, 0x103c0
	s_add_u32 s42, s42, 0x1800
	s_addc_u32 s43, s43, 0
	global_load_lds_dwordx4 v77, s[42:43]
	s_add_u32 m0, s48, 0x103c0
	s_add_u32 s44, s44, 0x1800
	s_addc_u32 s45, s45, 0
	global_load_lds_dwordx4 v78, s[44:45]
	s_waitcnt vmcnt(6)
	s_barrier
	s_add_u32 m0, s46, 0x0
	s_add_u32 s40, s40, 0x1800
	s_addc_u32 s41, s41, 0
	global_load_lds_dwordx4 v76, s[40:41]
	s_add_u32 m0, s47, 0x0
	s_add_u32 s42, s42, 0x1800
	s_addc_u32 s43, s43, 0
	global_load_lds_dwordx4 v77, s[42:43]
	s_add_u32 m0, s48, 0x0
	s_add_u32 s44, s44, 0x1800
	s_addc_u32 s45, s45, 0
	global_load_lds_dwordx4 v78, s[44:45]
	s_waitcnt vmcnt(6)
	s_barrier
	s_add_u32 m0, s46, 0x3000
	s_add_u32 s40, s40, 0x1800
	s_addc_u32 s41, s41, 0
	global_load_lds_dwordx4 v76, s[40:41]
	s_add_u32 m0, s47, 0x3000
	s_add_u32 s42, s42, 0x1800
	s_addc_u32 s43, s43, 0
	global_load_lds_dwordx4 v77, s[42:43]
	s_add_u32 m0, s48, 0x3000
	s_add_u32 s44, s44, 0x1800
	s_addc_u32 s45, s45, 0
	global_load_lds_dwordx4 v78, s[44:45]
	s_waitcnt vmcnt(6)
	s_barrier
	s_add_u32 m0, s46, 0xd3c0
	s_add_u32 s40, s40, 0x1800
	s_addc_u32 s41, s41, 0
	global_load_lds_dwordx4 v76, s[40:41]
	s_add_u32 m0, s47, 0xd3c0
	s_add_u32 s42, s42, 0x1800
	s_addc_u32 s43, s43, 0
	global_load_lds_dwordx4 v77, s[42:43]
	s_add_u32 m0, s48, 0xd3c0
	s_add_u32 s44, s44, 0x1800
	s_addc_u32 s45, s45, 0
	global_load_lds_dwordx4 v78, s[44:45]
	s_waitcnt vmcnt(6)
	s_barrier
	s_add_u32 m0, s46, 0x103c0
	s_add_u32 s40, s40, 0x1800
	s_addc_u32 s41, s41, 0
	global_load_lds_dwordx4 v76, s[40:41]
	s_add_u32 m0, s47, 0x103c0
	s_add_u32 s42, s42, 0x1800
	s_addc_u32 s43, s43, 0
	global_load_lds_dwordx4 v77, s[42:43]
	s_add_u32 m0, s48, 0x103c0
	s_add_u32 s44, s44, 0x1800
	s_addc_u32 s45, s45, 0
	global_load_lds_dwordx4 v78, s[44:45]
	s_waitcnt vmcnt(6)
	s_barrier
	s_add_u32 m0, s46, 0x0
	s_add_u32 s40, s40, 0x1800
	s_addc_u32 s41, s41, 0
	global_load_lds_dwordx4 v76, s[40:41]
	s_add_u32 m0, s47, 0x0
	s_add_u32 s42, s42, 0x1800
	s_addc_u32 s43, s43, 0
	global_load_lds_dwordx4 v77, s[42:43]
	s_add_u32 m0, s48, 0x0
	s_add_u32 s44, s44, 0x1800
	s_addc_u32 s45, s45, 0
	global_load_lds_dwordx4 v78, s[44:45]
	s_waitcnt vmcnt(6)
	s_barrier
	s_add_u32 m0, s46, 0x3000
	s_add_u32 s40, s40, 0x1800
	s_addc_u32 s41, s41, 0
	global_load_lds_dwordx4 v76, s[40:41]
	s_add_u32 m0, s47, 0x3000
	s_add_u32 s42, s42, 0x1800
	s_addc_u32 s43, s43, 0
	global_load_lds_dwordx4 v77, s[42:43]
	s_add_u32 m0, s48, 0x3000
	s_add_u32 s44, s44, 0x1800
	s_addc_u32 s45, s45, 0
	global_load_lds_dwordx4 v78, s[44:45]
	s_waitcnt vmcnt(6)
	s_barrier
	s_add_u32 m0, s46, 0xd3c0
	s_add_u32 s40, s40, 0x1800
	s_addc_u32 s41, s41, 0
	global_load_lds_dwordx4 v76, s[40:41]
	s_add_u32 m0, s47, 0xd3c0
	s_add_u32 s42, s42, 0x1800
	s_addc_u32 s43, s43, 0
	global_load_lds_dwordx4 v77, s[42:43]
	s_add_u32 m0, s48, 0xd3c0
	s_add_u32 s44, s44, 0x1800
	s_addc_u32 s45, s45, 0
	global_load_lds_dwordx4 v78, s[44:45]
	s_waitcnt vmcnt(6)
	s_barrier
	s_add_u32 m0, s46, 0x103c0
	s_add_u32 s40, s40, 0x1800
	s_addc_u32 s41, s41, 0
	global_load_lds_dwordx4 v76, s[40:41]
	s_add_u32 m0, s47, 0x103c0
	s_add_u32 s42, s42, 0x1800
	s_addc_u32 s43, s43, 0
	global_load_lds_dwordx4 v77, s[42:43]
	s_add_u32 m0, s48, 0x103c0
	s_add_u32 s44, s44, 0x1800
	s_addc_u32 s45, s45, 0
	global_load_lds_dwordx4 v78, s[44:45]
	s_waitcnt vmcnt(6)
	s_barrier
	s_add_u32 m0, s46, 0x0
	s_add_u32 s40, s40, 0x1800
	s_addc_u32 s41, s41, 0
	global_load_lds_dwordx4 v76, s[40:41]
	s_add_u32 m0, s47, 0x0
	s_add_u32 s42, s42, s49
	s_addc_u32 s43, s43, 0
	global_load_lds_dwordx4 v77, s[42:43]
	s_waitcnt vmcnt(5)
	s_barrier
	s_waitcnt vmcnt(2)
	s_barrier
	s_waitcnt vmcnt(0)
	s_barrier
	s_branch .LBB3_39
.LBB3_35:
	s_andn2_b64 vcc, exec, s[2:3]
	s_cbranch_vccnz .LBB3_39
	s_waitcnt vmcnt(4)
	v_ashrrev_i32_e32 v81, 31, v80
	v_lshl_add_u64 v[2:3], v[80:81], 3, s[20:21]
	v_add_co_u32_e32 v2, vcc, 0x48000, v2
	s_movk_i32 s8, 0x620
	s_nop 0
	v_addc_co_u32_e32 v3, vcc, 0, v3, vcc
	global_load_dwordx2 v[82:83], v[2:3], off
	v_and_b32_e32 v2, 0x70, v7
	v_bitop3_b32 v2, v0, v2, 48 bitop3:0x6c
	s_waitcnt vmcnt(4)
	v_mad_u64_u32 v[64:65], s[6:7], v9, s8, v[2:3]
	v_lshrrev_b32_e32 v3, 4, v92
	v_bitop3_b32 v3, v3, v0, 4 bitop3:0x36
	v_lshlrev_b32_e32 v3, 4, v3
	v_and_b32_e32 v4, 0x70, v3
	s_waitcnt vmcnt(3)
	v_mad_u64_u32 v[66:67], s[6:7], v8, s8, v[4:5]
	s_waitcnt vmcnt(2)
	v_mad_u64_u32 v[68:69], s[6:7], v6, s8, v[2:3]
	s_waitcnt vmcnt(1)
	v_mad_u64_u32 v[70:71], s[6:7], v1, s8, v[4:5]
	v_lshrrev_b32_e32 v85, 5, v92
	v_bfe_u32 v2, v0, 1, 3
	s_mov_b64 s[6:7], 0x1800
	s_add_u32 s4, s20, 0x4000000
	v_bitop3_b32 v32, v85, v2, 2 bitop3:0x36
	v_bitop3_b32 v33, v85, v2, 4 bitop3:0x36
	v_bitop3_b32 v34, v85, v2, 6 bitop3:0x36
	v_lshl_add_u64 v[2:3], v[86:87], 0, s[6:7]
	s_addc_u32 s5, s21, 0
	global_load_dwordx4 v[116:119], v64, s[4:5] offset:0
	global_load_dwordx4 v[120:123], v66, s[4:5] offset:0
	global_load_dwordx4 v[124:127], v68, s[4:5] offset:0
	global_load_dwordx4 v[128:131], v70, s[4:5] offset:0
	global_load_dwordx4 v[132:135], v64, s[4:5] offset:128
	global_load_dwordx4 v[136:139], v66, s[4:5] offset:128
	global_load_dwordx4 v[140:143], v68, s[4:5] offset:128
	global_load_dwordx4 v[144:147], v70, s[4:5] offset:128
	global_load_dwordx4 v[148:151], v64, s[4:5] offset:256
	global_load_dwordx4 v[152:155], v66, s[4:5] offset:256
	global_load_dwordx4 v[156:159], v68, s[4:5] offset:256
	global_load_dwordx4 v[72:75], v70, s[4:5] offset:256
	s_lshl_b32 s2, s27, 12
	s_addk_i32 s2, 0x6000
	v_lshrrev_b32_e32 v1, 1, v0
	v_or_b32_e32 v81, s2, v84
	v_lshlrev_b32_e32 v0, 7, v0
	v_and_b32_e32 v8, 0xf80, v0
	v_lshlrev_b32_e32 v9, 4, v32
	v_bitop3_b32 v1, v85, v1, 7 bitop3:0x78
	v_or3_b32 v96, s2, v9, v8
	v_lshlrev_b32_e32 v9, 4, v33
	v_lshlrev_b32_e32 v1, 4, v1
	v_or3_b32 v97, s2, v9, v8
	v_lshlrev_b32_e32 v9, 4, v34
	v_or3_b32 v95, s2, v1, v8
	v_or3_b32 v94, s2, v9, v8
	v_add_u32_e32 v98, 0x103c0, v84
	s_add_u32 m0, s46, 0x0
	s_nop 0
	global_load_lds_dwordx4 v76, s[40:41]
	s_add_u32 m0, s47, 0x0
	s_nop 0
	global_load_lds_dwordx4 v77, s[42:43]
	s_add_u32 m0, s48, 0x0
	s_nop 0
	global_load_lds_dwordx4 v78, s[44:45]
	s_add_u32 m0, s46, 0x3000
	s_add_u32 s40, s40, 0x1800
	s_addc_u32 s41, s41, 0
	global_load_lds_dwordx4 v76, s[40:41]
	s_add_u32 m0, s47, 0x3000
	s_add_u32 s42, s42, 0x1800
	s_addc_u32 s43, s43, 0
	global_load_lds_dwordx4 v77, s[42:43]
	s_add_u32 m0, s48, 0x3000
	s_add_u32 s44, s44, 0x1800
	s_addc_u32 s45, s45, 0
	global_load_lds_dwordx4 v78, s[44:45]
	s_add_u32 m0, s46, 0xd3c0
	s_add_u32 s40, s40, 0x1800
	s_addc_u32 s41, s41, 0
	global_load_lds_dwordx4 v76, s[40:41]
	s_add_u32 m0, s47, 0xd3c0
	s_add_u32 s42, s42, 0x1800
	s_addc_u32 s43, s43, 0
	global_load_lds_dwordx4 v77, s[42:43]
	s_add_u32 m0, s48, 0xd3c0
	s_add_u32 s44, s44, 0x1800
	s_addc_u32 s45, s45, 0
	global_load_lds_dwordx4 v78, s[44:45]
	s_add_u32 m0, s46, 0x103c0
	s_add_u32 s40, s40, 0x1800
	s_addc_u32 s41, s41, 0
	global_load_lds_dwordx4 v76, s[40:41]
	s_add_u32 m0, s47, 0x103c0
	s_add_u32 s42, s42, 0x1800
	s_addc_u32 s43, s43, 0
	global_load_lds_dwordx4 v77, s[42:43]
	s_add_u32 m0, s48, 0x103c0
	s_add_u32 s44, s44, 0x1800
	s_addc_u32 s45, s45, 0
	global_load_lds_dwordx4 v78, s[44:45]
	s_waitcnt vmcnt(20)
	ds_write_b128 v81, v[116:119]
	ds_write_b128 v81, v[120:123] offset:1024
	ds_write_b128 v81, v[124:127] offset:2048
	ds_write_b128 v81, v[128:131] offset:3072
	ds_read_b128 v[52:55], v95
	ds_read_b128 v[56:59], v96
	ds_read_b128 v[60:63], v97
	ds_read_b128 v[0:3], v94
	global_load_dwordx4 v[116:119], v64, s[4:5] offset:384
	global_load_dwordx4 v[120:123], v66, s[4:5] offset:384
	global_load_dwordx4 v[124:127], v68, s[4:5] offset:384
	global_load_dwordx4 v[128:131], v70, s[4:5] offset:384
	s_waitcnt vmcnt(13)
	s_waitcnt lgkmcnt(0)
	s_barrier
	ds_read_b128 v[4:7], v84 offset:0
	ds_read_b128 v[8:11], v84 offset:1024
	ds_read_b128 v[12:15], v84 offset:2048
	ds_read_b128 v[16:19], v84 offset:3072
	ds_read_b128 v[20:23], v84 offset:4096
	ds_read_b128 v[24:27], v84 offset:5120
	ds_read_b128 v[28:31], v84 offset:6144
	ds_read_b128 v[32:35], v84 offset:7168
	ds_read_b128 v[36:39], v84 offset:8192
	ds_read_b128 v[40:43], v84 offset:9216
	ds_read_b128 v[44:47], v84 offset:10240
	ds_read_b128 v[48:51], v84 offset:11264
	s_waitcnt lgkmcnt(6)
	v_mfma_f32_32x32x16_f16 a[80:95], v[4:7], v[52:55], 0
	v_mfma_f32_32x32x16_f16 a[64:79], v[8:11], v[52:55], 0
	v_mfma_f32_32x32x16_f16 a[48:63], v[12:15], v[52:55], 0
	s_waitcnt vmcnt(10)
	s_waitcnt lgkmcnt(0)
	s_barrier
	ds_read_b128 v[4:7], v84 offset:12288
	ds_read_b128 v[8:11], v84 offset:13312
	ds_read_b128 v[12:15], v84 offset:14336
	v_mfma_f32_32x32x16_f16 a[32:47], v[16:19], v[52:55], 0
	ds_read_b128 v[16:19], v84 offset:15360
	v_mfma_f32_32x32x16_f16 a[16:31], v[20:23], v[52:55], 0
	ds_read_b128 v[20:23], v84 offset:16384
	v_mfma_f32_32x32x16_f16 a[0:15], v[24:27], v[52:55], 0
	ds_read_b128 v[24:27], v84 offset:17408
	v_mfma_f32_32x32x16_f16 a[80:95], v[28:31], v[56:59], a[80:95]
	s_add_u32 m0, s46, 0x0
	s_add_u32 s40, s40, 0x1800
	s_addc_u32 s41, s41, 0
	global_load_lds_dwordx4 v76, s[40:41]
	ds_read_b128 v[28:31], v84 offset:18432
	v_mfma_f32_32x32x16_f16 a[64:79], v[32:35], v[56:59], a[64:79]
	ds_read_b128 v[32:35], v84 offset:19456
	v_mfma_f32_32x32x16_f16 a[48:63], v[36:39], v[56:59], a[48:63]
	s_add_u32 m0, s47, 0x0
	s_add_u32 s42, s42, 0x1800
	s_addc_u32 s43, s43, 0
	global_load_lds_dwordx4 v77, s[42:43]
	ds_read_b128 v[36:39], v84 offset:20480
	v_mfma_f32_32x32x16_f16 a[32:47], v[40:43], v[56:59], a[32:47]
	ds_read_b128 v[40:43], v84 offset:21504
	v_mfma_f32_32x32x16_f16 a[16:31], v[44:47], v[56:59], a[16:31]
	s_add_u32 m0, s48, 0x0
	s_add_u32 s44, s44, 0x1800
	s_addc_u32 s45, s45, 0
	global_load_lds_dwordx4 v78, s[44:45]
	ds_read_b128 v[44:47], v84 offset:22528
	v_mfma_f32_32x32x16_f16 a[0:15], v[48:51], v[56:59], a[0:15]
	ds_read_b128 v[48:51], v84 offset:23552
	s_waitcnt lgkmcnt(6)
	v_mfma_f32_32x32x16_f16 a[80:95], v[4:7], v[60:63], a[80:95]
	s_waitcnt vmcnt(23)
	ds_write_b128 v81, v[132:135]
	ds_write_b128 v81, v[136:139] offset:1024
	v_mfma_f32_32x32x16_f16 a[64:79], v[8:11], v[60:63], a[64:79]
	ds_write_b128 v81, v[140:143] offset:2048
	ds_write_b128 v81, v[144:147] offset:3072
	v_mfma_f32_32x32x16_f16 a[48:63], v[12:15], v[60:63], a[48:63]
	ds_read_b128 v[100:103], v95
	ds_read_b128 v[104:107], v96
	ds_read_b128 v[108:111], v97
	ds_read_b128 v[112:115], v94
	s_waitcnt vmcnt(10)
	s_waitcnt lgkmcnt(8)
	s_barrier
	ds_read_b128 v[4:7], v84 offset:54208
	ds_read_b128 v[8:11], v84 offset:55232
	ds_read_b128 v[12:15], v84 offset:56256
	v_mfma_f32_32x32x16_f16 a[32:47], v[16:19], v[60:63], a[32:47]
	ds_read_b128 v[16:19], v84 offset:57280
	v_mfma_f32_32x32x16_f16 a[16:31], v[20:23], v[60:63], a[16:31]
	ds_read_b128 v[20:23], v84 offset:58304
	v_mfma_f32_32x32x16_f16 a[0:15], v[24:27], v[60:63], a[0:15]
	ds_read_b128 v[24:27], v84 offset:59328
	s_waitcnt lgkmcnt(6)
	v_mfma_f32_32x32x16_f16 a[80:95], v[28:31], v[0:3], a[80:95]
	s_add_u32 m0, s46, 0x3000
	s_add_u32 s40, s40, 0x1800
	s_addc_u32 s41, s41, 0
	global_load_lds_dwordx4 v76, s[40:41]
	ds_read_b128 v[28:31], v84 offset:60352
	v_mfma_f32_32x32x16_f16 a[64:79], v[32:35], v[0:3], a[64:79]
	global_load_dwordx4 v[132:135], v64, s[4:5] offset:512
	global_load_dwordx4 v[136:139], v66, s[4:5] offset:512
	ds_read_b128 v[32:35], v84 offset:61376
	v_mfma_f32_32x32x16_f16 a[48:63], v[36:39], v[0:3], a[48:63]
	s_add_u32 m0, s47, 0x3000
	s_add_u32 s42, s42, 0x1800
	s_addc_u32 s43, s43, 0
	global_load_lds_dwordx4 v77, s[42:43]
	ds_read_b128 v[36:39], v84 offset:62400
	v_mfma_f32_32x32x16_f16 a[32:47], v[40:43], v[0:3], a[32:47]
	global_load_dwordx4 v[140:143], v68, s[4:5] offset:512
	global_load_dwordx4 v[144:147], v70, s[4:5] offset:512
	ds_read_b128 v[40:43], v84 offset:63424
	v_mfma_f32_32x32x16_f16 a[16:31], v[44:47], v[0:3], a[16:31]
	s_add_u32 m0, s48, 0x3000
	s_add_u32 s44, s44, 0x1800
	s_addc_u32 s45, s45, 0
	global_load_lds_dwordx4 v78, s[44:45]
	ds_read_b128 v[44:47], v84 offset:64448
	v_mfma_f32_32x32x16_f16 a[0:15], v[48:51], v[0:3], a[0:15]
	ds_read_b128 v[48:51], v84 offset:65472
	s_waitcnt lgkmcnt(6)
	v_mfma_f32_32x32x16_f16 a[80:95], v[4:7], v[100:103], a[80:95]
	v_mfma_f32_32x32x16_f16 a[64:79], v[8:11], v[100:103], a[64:79]
	v_mfma_f32_32x32x16_f16 a[48:63], v[12:15], v[100:103], a[48:63]
	s_waitcnt vmcnt(14)
	s_waitcnt lgkmcnt(0)
	s_barrier
	ds_read_b128 v[4:7], v98
	ds_read_b128 v[8:11], v98 offset:1024
	ds_read_b128 v[12:15], v98 offset:2048
	v_mfma_f32_32x32x16_f16 a[32:47], v[16:19], v[100:103], a[32:47]
	ds_read_b128 v[16:19], v98 offset:3072
	v_mfma_f32_32x32x16_f16 a[16:31], v[20:23], v[100:103], a[16:31]
	ds_read_b128 v[20:23], v98 offset:4096
	v_mfma_f32_32x32x16_f16 a[0:15], v[24:27], v[100:103], a[0:15]
	ds_read_b128 v[24:27], v98 offset:5120
	v_mfma_f32_32x32x16_f16 a[80:95], v[28:31], v[104:107], a[80:95]
	s_add_u32 m0, s46, 0xd3c0
	s_add_u32 s40, s40, 0x1800
	s_addc_u32 s41, s41, 0
	global_load_lds_dwordx4 v76, s[40:41]
	ds_read_b128 v[28:31], v98 offset:6144
	v_mfma_f32_32x32x16_f16 a[64:79], v[32:35], v[104:107], a[64:79]
	ds_read_b128 v[32:35], v98 offset:7168
	v_mfma_f32_32x32x16_f16 a[48:63], v[36:39], v[104:107], a[48:63]
	s_add_u32 m0, s47, 0xd3c0
	s_add_u32 s42, s42, 0x1800
	s_addc_u32 s43, s43, 0
	global_load_lds_dwordx4 v77, s[42:43]
	ds_read_b128 v[36:39], v98 offset:8192
	v_mfma_f32_32x32x16_f16 a[32:47], v[40:43], v[104:107], a[32:47]
	ds_read_b128 v[40:43], v98 offset:9216
	v_mfma_f32_32x32x16_f16 a[16:31], v[44:47], v[104:107], a[16:31]
	s_add_u32 m0, s48, 0xd3c0
	s_add_u32 s44, s44, 0x1800
	s_addc_u32 s45, s45, 0
	global_load_lds_dwordx4 v78, s[44:45]
	ds_read_b128 v[44:47], v98 offset:10240
	v_mfma_f32_32x32x16_f16 a[0:15], v[48:51], v[104:107], a[0:15]
	ds_read_b128 v[48:51], v98 offset:11264
	s_waitcnt lgkmcnt(6)
	v_mfma_f32_32x32x16_f16 a[80:95], v[4:7], v[108:111], a[80:95]
	s_waitcnt vmcnt(29)
	ds_write_b128 v81, v[148:151]
	ds_write_b128 v81, v[152:155] offset:1024
	v_mfma_f32_32x32x16_f16 a[64:79], v[8:11], v[108:111], a[64:79]
	ds_write_b128 v81, v[156:159] offset:2048
	ds_write_b128 v81, v[72:75] offset:3072
	v_mfma_f32_32x32x16_f16 a[48:63], v[12:15], v[108:111], a[48:63]
	ds_read_b128 v[52:55], v95
	ds_read_b128 v[56:59], v96
	ds_read_b128 v[60:63], v97
	ds_read_b128 v[0:3], v94
	s_waitcnt vmcnt(10)
	s_waitcnt lgkmcnt(8)
	s_barrier
	ds_read_b128 v[4:7], v84 offset:0
	ds_read_b128 v[8:11], v84 offset:1024
	ds_read_b128 v[12:15], v84 offset:2048
	v_mfma_f32_32x32x16_f16 a[32:47], v[16:19], v[108:111], a[32:47]
	ds_read_b128 v[16:19], v84 offset:3072
	v_mfma_f32_32x32x16_f16 a[16:31], v[20:23], v[108:111], a[16:31]
	ds_read_b128 v[20:23], v84 offset:4096
	v_mfma_f32_32x32x16_f16 a[0:15], v[24:27], v[108:111], a[0:15]
	ds_read_b128 v[24:27], v84 offset:5120
	s_waitcnt lgkmcnt(6)
	v_mfma_f32_32x32x16_f16 a[80:95], v[28:31], v[112:115], a[80:95]
	s_add_u32 m0, s46, 0x103c0
	s_add_u32 s40, s40, 0x1800
	s_addc_u32 s41, s41, 0
	global_load_lds_dwordx4 v76, s[40:41]
	ds_read_b128 v[28:31], v84 offset:6144
	v_mfma_f32_32x32x16_f16 a[64:79], v[32:35], v[112:115], a[64:79]
	global_load_dwordx4 v[148:151], v64, s[4:5] offset:640
	global_load_dwordx4 v[152:155], v66, s[4:5] offset:640
	ds_read_b128 v[32:35], v84 offset:7168
	v_mfma_f32_32x32x16_f16 a[48:63], v[36:39], v[112:115], a[48:63]
	s_add_u32 m0, s47, 0x103c0
	s_add_u32 s42, s42, 0x1800
	s_addc_u32 s43, s43, 0
	global_load_lds_dwordx4 v77, s[42:43]
	ds_read_b128 v[36:39], v84 offset:8192
	v_mfma_f32_32x32x16_f16 a[32:47], v[40:43], v[112:115], a[32:47]
	global_load_dwordx4 v[156:159], v68, s[4:5] offset:640
	global_load_dwordx4 v[72:75], v70, s[4:5] offset:640
	ds_read_b128 v[40:43], v84 offset:9216
	v_mfma_f32_32x32x16_f16 a[16:31], v[44:47], v[112:115], a[16:31]
	s_add_u32 m0, s48, 0x103c0
	s_add_u32 s44, s44, 0x1800
	s_addc_u32 s45, s45, 0
	global_load_lds_dwordx4 v78, s[44:45]
	ds_read_b128 v[44:47], v84 offset:10240
	v_mfma_f32_32x32x16_f16 a[0:15], v[48:51], v[112:115], a[0:15]
	ds_read_b128 v[48:51], v84 offset:11264
	s_waitcnt lgkmcnt(6)
	v_mfma_f32_32x32x16_f16 a[80:95], v[4:7], v[52:55], a[80:95]
	v_mfma_f32_32x32x16_f16 a[64:79], v[8:11], v[52:55], a[64:79]
	v_mfma_f32_32x32x16_f16 a[48:63], v[12:15], v[52:55], a[48:63]
	s_waitcnt vmcnt(10)
	s_waitcnt lgkmcnt(0)
	s_barrier
	ds_read_b128 v[4:7], v84 offset:12288
	ds_read_b128 v[8:11], v84 offset:13312
	ds_read_b128 v[12:15], v84 offset:14336
	v_mfma_f32_32x32x16_f16 a[32:47], v[16:19], v[52:55], a[32:47]
	ds_read_b128 v[16:19], v84 offset:15360
	v_mfma_f32_32x32x16_f16 a[16:31], v[20:23], v[52:55], a[16:31]
	ds_read_b128 v[20:23], v84 offset:16384
	v_mfma_f32_32x32x16_f16 a[0:15], v[24:27], v[52:55], a[0:15]
	ds_read_b128 v[24:27], v84 offset:17408
	v_mfma_f32_32x32x16_f16 a[80:95], v[28:31], v[56:59], a[80:95]
	s_add_u32 m0, s46, 0x0
	s_add_u32 s40, s40, 0x1800
	s_addc_u32 s41, s41, 0
	global_load_lds_dwordx4 v76, s[40:41]
	ds_read_b128 v[28:31], v84 offset:18432
	v_mfma_f32_32x32x16_f16 a[64:79], v[32:35], v[56:59], a[64:79]
	ds_read_b128 v[32:35], v84 offset:19456
	v_mfma_f32_32x32x16_f16 a[48:63], v[36:39], v[56:59], a[48:63]
	s_add_u32 m0, s47, 0x0
	s_add_u32 s42, s42, 0x1800
	s_addc_u32 s43, s43, 0
	global_load_lds_dwordx4 v77, s[42:43]
	ds_read_b128 v[36:39], v84 offset:20480
	v_mfma_f32_32x32x16_f16 a[32:47], v[40:43], v[56:59], a[32:47]
	ds_read_b128 v[40:43], v84 offset:21504
	v_mfma_f32_32x32x16_f16 a[16:31], v[44:47], v[56:59], a[16:31]
	s_add_u32 m0, s48, 0x0
	s_add_u32 s44, s44, 0x1800
	s_addc_u32 s45, s45, 0
	global_load_lds_dwordx4 v78, s[44:45]
	ds_read_b128 v[44:47], v84 offset:22528
	v_mfma_f32_32x32x16_f16 a[0:15], v[48:51], v[56:59], a[0:15]
	ds_read_b128 v[48:51], v84 offset:23552
	s_waitcnt lgkmcnt(6)
	v_mfma_f32_32x32x16_f16 a[80:95], v[4:7], v[60:63], a[80:95]
	s_waitcnt vmcnt(23)
	ds_write_b128 v81, v[116:119]
	ds_write_b128 v81, v[120:123] offset:1024
	v_mfma_f32_32x32x16_f16 a[64:79], v[8:11], v[60:63], a[64:79]
	ds_write_b128 v81, v[124:127] offset:2048
	ds_write_b128 v81, v[128:131] offset:3072
	v_mfma_f32_32x32x16_f16 a[48:63], v[12:15], v[60:63], a[48:63]
	ds_read_b128 v[100:103], v95
	ds_read_b128 v[104:107], v96
	ds_read_b128 v[108:111], v97
	ds_read_b128 v[112:115], v94
	s_waitcnt vmcnt(10)
	s_waitcnt lgkmcnt(8)
	s_barrier
	ds_read_b128 v[4:7], v84 offset:54208
	ds_read_b128 v[8:11], v84 offset:55232
	ds_read_b128 v[12:15], v84 offset:56256
	v_mfma_f32_32x32x16_f16 a[32:47], v[16:19], v[60:63], a[32:47]
	ds_read_b128 v[16:19], v84 offset:57280
	v_mfma_f32_32x32x16_f16 a[16:31], v[20:23], v[60:63], a[16:31]
	ds_read_b128 v[20:23], v84 offset:58304
	v_mfma_f32_32x32x16_f16 a[0:15], v[24:27], v[60:63], a[0:15]
	ds_read_b128 v[24:27], v84 offset:59328
	s_waitcnt lgkmcnt(6)
	v_mfma_f32_32x32x16_f16 a[80:95], v[28:31], v[0:3], a[80:95]
	s_add_u32 m0, s46, 0x3000
	s_add_u32 s40, s40, 0x1800
	s_addc_u32 s41, s41, 0
	global_load_lds_dwordx4 v76, s[40:41]
	ds_read_b128 v[28:31], v84 offset:60352
	v_mfma_f32_32x32x16_f16 a[64:79], v[32:35], v[0:3], a[64:79]
	global_load_dwordx4 v[116:119], v64, s[4:5] offset:768
	global_load_dwordx4 v[120:123], v66, s[4:5] offset:768
	ds_read_b128 v[32:35], v84 offset:61376
	v_mfma_f32_32x32x16_f16 a[48:63], v[36:39], v[0:3], a[48:63]
	s_add_u32 m0, s47, 0x3000
	s_add_u32 s42, s42, 0x1800
	s_addc_u32 s43, s43, 0
	global_load_lds_dwordx4 v77, s[42:43]
	ds_read_b128 v[36:39], v84 offset:62400
	v_mfma_f32_32x32x16_f16 a[32:47], v[40:43], v[0:3], a[32:47]
	global_load_dwordx4 v[124:127], v68, s[4:5] offset:768
	global_load_dwordx4 v[128:131], v70, s[4:5] offset:768
	ds_read_b128 v[40:43], v84 offset:63424
	v_mfma_f32_32x32x16_f16 a[16:31], v[44:47], v[0:3], a[16:31]
	s_add_u32 m0, s48, 0x3000
	s_add_u32 s44, s44, 0x1800
	s_addc_u32 s45, s45, 0
	global_load_lds_dwordx4 v78, s[44:45]
	ds_read_b128 v[44:47], v84 offset:64448
	v_mfma_f32_32x32x16_f16 a[0:15], v[48:51], v[0:3], a[0:15]
	ds_read_b128 v[48:51], v84 offset:65472
	s_waitcnt lgkmcnt(6)
	v_mfma_f32_32x32x16_f16 a[80:95], v[4:7], v[100:103], a[80:95]
	v_mfma_f32_32x32x16_f16 a[64:79], v[8:11], v[100:103], a[64:79]
	v_mfma_f32_32x32x16_f16 a[48:63], v[12:15], v[100:103], a[48:63]
	s_waitcnt vmcnt(10)
	s_waitcnt lgkmcnt(0)
	s_barrier
	ds_read_b128 v[4:7], v98
	ds_read_b128 v[8:11], v98 offset:1024
	ds_read_b128 v[12:15], v98 offset:2048
	v_mfma_f32_32x32x16_f16 a[32:47], v[16:19], v[100:103], a[32:47]
	ds_read_b128 v[16:19], v98 offset:3072
	v_mfma_f32_32x32x16_f16 a[16:31], v[20:23], v[100:103], a[16:31]
	ds_read_b128 v[20:23], v98 offset:4096
	v_mfma_f32_32x32x16_f16 a[0:15], v[24:27], v[100:103], a[0:15]
	ds_read_b128 v[24:27], v98 offset:5120
	v_mfma_f32_32x32x16_f16 a[80:95], v[28:31], v[104:107], a[80:95]
	s_add_u32 m0, s46, 0xd3c0
	s_add_u32 s40, s40, 0x1800
	s_addc_u32 s41, s41, 0
	global_load_lds_dwordx4 v76, s[40:41]
	ds_read_b128 v[28:31], v98 offset:6144
	v_mfma_f32_32x32x16_f16 a[64:79], v[32:35], v[104:107], a[64:79]
	ds_read_b128 v[32:35], v98 offset:7168
	v_mfma_f32_32x32x16_f16 a[48:63], v[36:39], v[104:107], a[48:63]
	s_add_u32 m0, s47, 0xd3c0
	s_add_u32 s42, s42, 0x1800
	s_addc_u32 s43, s43, 0
	global_load_lds_dwordx4 v77, s[42:43]
	ds_read_b128 v[36:39], v98 offset:8192
	v_mfma_f32_32x32x16_f16 a[32:47], v[40:43], v[104:107], a[32:47]
	ds_read_b128 v[40:43], v98 offset:9216
	v_mfma_f32_32x32x16_f16 a[16:31], v[44:47], v[104:107], a[16:31]
	s_add_u32 m0, s48, 0xd3c0
	s_add_u32 s44, s44, 0x1800
	s_addc_u32 s45, s45, 0
	global_load_lds_dwordx4 v78, s[44:45]
	ds_read_b128 v[44:47], v98 offset:10240
	v_mfma_f32_32x32x16_f16 a[0:15], v[48:51], v[104:107], a[0:15]
	ds_read_b128 v[48:51], v98 offset:11264
	s_waitcnt lgkmcnt(6)
	v_mfma_f32_32x32x16_f16 a[80:95], v[4:7], v[108:111], a[80:95]
	s_waitcnt vmcnt(24)
	ds_write_b128 v81, v[132:135]
	ds_write_b128 v81, v[136:139] offset:1024
	v_mfma_f32_32x32x16_f16 a[64:79], v[8:11], v[108:111], a[64:79]
	ds_write_b128 v81, v[140:143] offset:2048
	ds_write_b128 v81, v[144:147] offset:3072
	v_mfma_f32_32x32x16_f16 a[48:63], v[12:15], v[108:111], a[48:63]
	ds_read_b128 v[52:55], v95
	ds_read_b128 v[56:59], v96
	ds_read_b128 v[60:63], v97
	ds_read_b128 v[0:3], v94
	s_waitcnt vmcnt(10)
	s_waitcnt lgkmcnt(8)
	s_barrier
	ds_read_b128 v[4:7], v84 offset:0
	ds_read_b128 v[8:11], v84 offset:1024
	ds_read_b128 v[12:15], v84 offset:2048
	v_mfma_f32_32x32x16_f16 a[32:47], v[16:19], v[108:111], a[32:47]
	ds_read_b128 v[16:19], v84 offset:3072
	v_mfma_f32_32x32x16_f16 a[16:31], v[20:23], v[108:111], a[16:31]
	ds_read_b128 v[20:23], v84 offset:4096
	v_mfma_f32_32x32x16_f16 a[0:15], v[24:27], v[108:111], a[0:15]
	ds_read_b128 v[24:27], v84 offset:5120
	s_waitcnt lgkmcnt(6)
	v_mfma_f32_32x32x16_f16 a[80:95], v[28:31], v[112:115], a[80:95]
	s_add_u32 m0, s46, 0x103c0
	s_add_u32 s40, s40, 0x1800
	s_addc_u32 s41, s41, 0
	global_load_lds_dwordx4 v76, s[40:41]
	ds_read_b128 v[28:31], v84 offset:6144
	v_mfma_f32_32x32x16_f16 a[64:79], v[32:35], v[112:115], a[64:79]
	global_load_dwordx4 v[132:135], v64, s[4:5] offset:896
	global_load_dwordx4 v[136:139], v66, s[4:5] offset:896
	ds_read_b128 v[32:35], v84 offset:7168
	v_mfma_f32_32x32x16_f16 a[48:63], v[36:39], v[112:115], a[48:63]
	s_add_u32 m0, s47, 0x103c0
	s_add_u32 s42, s42, 0x1800
	s_addc_u32 s43, s43, 0
	global_load_lds_dwordx4 v77, s[42:43]
	ds_read_b128 v[36:39], v84 offset:8192
	v_mfma_f32_32x32x16_f16 a[32:47], v[40:43], v[112:115], a[32:47]
	global_load_dwordx4 v[140:143], v68, s[4:5] offset:896
	global_load_dwordx4 v[144:147], v70, s[4:5] offset:896
	ds_read_b128 v[40:43], v84 offset:9216
	v_mfma_f32_32x32x16_f16 a[16:31], v[44:47], v[112:115], a[16:31]
	s_add_u32 m0, s48, 0x103c0
	s_add_u32 s44, s44, 0x1800
	s_addc_u32 s45, s45, 0
	global_load_lds_dwordx4 v78, s[44:45]
	ds_read_b128 v[44:47], v84 offset:10240
	v_mfma_f32_32x32x16_f16 a[0:15], v[48:51], v[112:115], a[0:15]
	ds_read_b128 v[48:51], v84 offset:11264
	s_waitcnt lgkmcnt(6)
	v_mfma_f32_32x32x16_f16 a[80:95], v[4:7], v[52:55], a[80:95]
	v_mfma_f32_32x32x16_f16 a[64:79], v[8:11], v[52:55], a[64:79]
	v_mfma_f32_32x32x16_f16 a[48:63], v[12:15], v[52:55], a[48:63]
	s_waitcnt vmcnt(10)
	s_waitcnt lgkmcnt(0)
	s_barrier
	ds_read_b128 v[4:7], v84 offset:12288
	ds_read_b128 v[8:11], v84 offset:13312
	ds_read_b128 v[12:15], v84 offset:14336
	v_mfma_f32_32x32x16_f16 a[32:47], v[16:19], v[52:55], a[32:47]
	ds_read_b128 v[16:19], v84 offset:15360
	v_mfma_f32_32x32x16_f16 a[16:31], v[20:23], v[52:55], a[16:31]
	ds_read_b128 v[20:23], v84 offset:16384
	v_mfma_f32_32x32x16_f16 a[0:15], v[24:27], v[52:55], a[0:15]
	ds_read_b128 v[24:27], v84 offset:17408
	v_mfma_f32_32x32x16_f16 a[80:95], v[28:31], v[56:59], a[80:95]
	s_add_u32 m0, s46, 0x0
	s_add_u32 s40, s40, 0x1800
	s_addc_u32 s41, s41, 0
	global_load_lds_dwordx4 v76, s[40:41]
	ds_read_b128 v[28:31], v84 offset:18432
	v_mfma_f32_32x32x16_f16 a[64:79], v[32:35], v[56:59], a[64:79]
	ds_read_b128 v[32:35], v84 offset:19456
	v_mfma_f32_32x32x16_f16 a[48:63], v[36:39], v[56:59], a[48:63]
	s_add_u32 m0, s47, 0x0
	s_add_u32 s42, s42, 0x1800
	s_addc_u32 s43, s43, 0
	global_load_lds_dwordx4 v77, s[42:43]
	ds_read_b128 v[36:39], v84 offset:20480
	v_mfma_f32_32x32x16_f16 a[32:47], v[40:43], v[56:59], a[32:47]
	ds_read_b128 v[40:43], v84 offset:21504
	v_mfma_f32_32x32x16_f16 a[16:31], v[44:47], v[56:59], a[16:31]
	s_add_u32 m0, s48, 0x0
	s_add_u32 s44, s44, 0x1800
	s_addc_u32 s45, s45, 0
	global_load_lds_dwordx4 v78, s[44:45]
	ds_read_b128 v[44:47], v84 offset:22528
	v_mfma_f32_32x32x16_f16 a[0:15], v[48:51], v[56:59], a[0:15]
	ds_read_b128 v[48:51], v84 offset:23552
	s_waitcnt lgkmcnt(6)
	v_mfma_f32_32x32x16_f16 a[80:95], v[4:7], v[60:63], a[80:95]
	s_waitcnt vmcnt(24)
	ds_write_b128 v81, v[148:151]
	ds_write_b128 v81, v[152:155] offset:1024
	v_mfma_f32_32x32x16_f16 a[64:79], v[8:11], v[60:63], a[64:79]
	ds_write_b128 v81, v[156:159] offset:2048
	ds_write_b128 v81, v[72:75] offset:3072
	v_mfma_f32_32x32x16_f16 a[48:63], v[12:15], v[60:63], a[48:63]
	ds_read_b128 v[100:103], v95
	ds_read_b128 v[104:107], v96
	ds_read_b128 v[108:111], v97
	ds_read_b128 v[112:115], v94
	s_waitcnt vmcnt(10)
	s_waitcnt lgkmcnt(8)
	s_barrier
	ds_read_b128 v[4:7], v84 offset:54208
	ds_read_b128 v[8:11], v84 offset:55232
	ds_read_b128 v[12:15], v84 offset:56256
	v_mfma_f32_32x32x16_f16 a[32:47], v[16:19], v[60:63], a[32:47]
	ds_read_b128 v[16:19], v84 offset:57280
	v_mfma_f32_32x32x16_f16 a[16:31], v[20:23], v[60:63], a[16:31]
	ds_read_b128 v[20:23], v84 offset:58304
	v_mfma_f32_32x32x16_f16 a[0:15], v[24:27], v[60:63], a[0:15]
	ds_read_b128 v[24:27], v84 offset:59328
	s_waitcnt lgkmcnt(6)
	v_mfma_f32_32x32x16_f16 a[80:95], v[28:31], v[0:3], a[80:95]
	s_add_u32 m0, s46, 0x3000
	s_add_u32 s40, s40, 0x1800
	s_addc_u32 s41, s41, 0
	global_load_lds_dwordx4 v76, s[40:41]
	ds_read_b128 v[28:31], v84 offset:60352
	v_mfma_f32_32x32x16_f16 a[64:79], v[32:35], v[0:3], a[64:79]
	global_load_dwordx4 v[148:151], v64, s[4:5] offset:1024
	global_load_dwordx4 v[152:155], v66, s[4:5] offset:1024
	ds_read_b128 v[32:35], v84 offset:61376
	v_mfma_f32_32x32x16_f16 a[48:63], v[36:39], v[0:3], a[48:63]
	s_add_u32 m0, s47, 0x3000
	s_add_u32 s42, s42, 0x1800
	s_addc_u32 s43, s43, 0
	global_load_lds_dwordx4 v77, s[42:43]
	ds_read_b128 v[36:39], v84 offset:62400
	v_mfma_f32_32x32x16_f16 a[32:47], v[40:43], v[0:3], a[32:47]
	global_load_dwordx4 v[156:159], v68, s[4:5] offset:1024
	global_load_dwordx4 v[72:75], v70, s[4:5] offset:1024
	ds_read_b128 v[40:43], v84 offset:63424
	v_mfma_f32_32x32x16_f16 a[16:31], v[44:47], v[0:3], a[16:31]
	s_add_u32 m0, s48, 0x3000
	s_add_u32 s44, s44, 0x1800
	s_addc_u32 s45, s45, 0
	global_load_lds_dwordx4 v78, s[44:45]
	ds_read_b128 v[44:47], v84 offset:64448
	v_mfma_f32_32x32x16_f16 a[0:15], v[48:51], v[0:3], a[0:15]
	ds_read_b128 v[48:51], v84 offset:65472
	s_waitcnt lgkmcnt(6)
	v_mfma_f32_32x32x16_f16 a[80:95], v[4:7], v[100:103], a[80:95]
	v_mfma_f32_32x32x16_f16 a[64:79], v[8:11], v[100:103], a[64:79]
	v_mfma_f32_32x32x16_f16 a[48:63], v[12:15], v[100:103], a[48:63]
	s_waitcnt vmcnt(10)
	s_waitcnt lgkmcnt(0)
	s_barrier
	ds_read_b128 v[4:7], v98
	ds_read_b128 v[8:11], v98 offset:1024
	ds_read_b128 v[12:15], v98 offset:2048
	v_mfma_f32_32x32x16_f16 a[32:47], v[16:19], v[100:103], a[32:47]
	ds_read_b128 v[16:19], v98 offset:3072
	v_mfma_f32_32x32x16_f16 a[16:31], v[20:23], v[100:103], a[16:31]
	ds_read_b128 v[20:23], v98 offset:4096
	v_mfma_f32_32x32x16_f16 a[0:15], v[24:27], v[100:103], a[0:15]
	ds_read_b128 v[24:27], v98 offset:5120
	v_mfma_f32_32x32x16_f16 a[80:95], v[28:31], v[104:107], a[80:95]
	s_add_u32 m0, s46, 0xd3c0
	s_add_u32 s40, s40, 0x1800
	s_addc_u32 s41, s41, 0
	global_load_lds_dwordx4 v76, s[40:41]
	ds_read_b128 v[28:31], v98 offset:6144
	v_mfma_f32_32x32x16_f16 a[64:79], v[32:35], v[104:107], a[64:79]
	ds_read_b128 v[32:35], v98 offset:7168
	v_mfma_f32_32x32x16_f16 a[48:63], v[36:39], v[104:107], a[48:63]
	s_add_u32 m0, s47, 0xd3c0
	s_add_u32 s42, s42, 0x1800
	s_addc_u32 s43, s43, 0
	global_load_lds_dwordx4 v77, s[42:43]
	ds_read_b128 v[36:39], v98 offset:8192
	v_mfma_f32_32x32x16_f16 a[32:47], v[40:43], v[104:107], a[32:47]
	ds_read_b128 v[40:43], v98 offset:9216
	v_mfma_f32_32x32x16_f16 a[16:31], v[44:47], v[104:107], a[16:31]
	s_add_u32 m0, s48, 0xd3c0
	s_add_u32 s44, s44, 0x1800
	s_addc_u32 s45, s45, 0
	global_load_lds_dwordx4 v78, s[44:45]
	ds_read_b128 v[44:47], v98 offset:10240
	v_mfma_f32_32x32x16_f16 a[0:15], v[48:51], v[104:107], a[0:15]
	ds_read_b128 v[48:51], v98 offset:11264
	s_waitcnt lgkmcnt(6)
	v_mfma_f32_32x32x16_f16 a[80:95], v[4:7], v[108:111], a[80:95]
	s_waitcnt vmcnt(24)
	ds_write_b128 v81, v[116:119]
	ds_write_b128 v81, v[120:123] offset:1024
	v_mfma_f32_32x32x16_f16 a[64:79], v[8:11], v[108:111], a[64:79]
	ds_write_b128 v81, v[124:127] offset:2048
	ds_write_b128 v81, v[128:131] offset:3072
	v_mfma_f32_32x32x16_f16 a[48:63], v[12:15], v[108:111], a[48:63]
	ds_read_b128 v[52:55], v95
	ds_read_b128 v[56:59], v96
	ds_read_b128 v[60:63], v97
	ds_read_b128 v[0:3], v94
	s_waitcnt vmcnt(10)
	s_waitcnt lgkmcnt(8)
	s_barrier
	ds_read_b128 v[4:7], v84 offset:0
	ds_read_b128 v[8:11], v84 offset:1024
	ds_read_b128 v[12:15], v84 offset:2048
	v_mfma_f32_32x32x16_f16 a[32:47], v[16:19], v[108:111], a[32:47]
	ds_read_b128 v[16:19], v84 offset:3072
	v_mfma_f32_32x32x16_f16 a[16:31], v[20:23], v[108:111], a[16:31]
	ds_read_b128 v[20:23], v84 offset:4096
	v_mfma_f32_32x32x16_f16 a[0:15], v[24:27], v[108:111], a[0:15]
	ds_read_b128 v[24:27], v84 offset:5120
	s_waitcnt lgkmcnt(6)
	v_mfma_f32_32x32x16_f16 a[80:95], v[28:31], v[112:115], a[80:95]
	s_add_u32 m0, s46, 0x103c0
	s_add_u32 s40, s40, 0x1800
	s_addc_u32 s41, s41, 0
	global_load_lds_dwordx4 v76, s[40:41]
	ds_read_b128 v[28:31], v84 offset:6144
	v_mfma_f32_32x32x16_f16 a[64:79], v[32:35], v[112:115], a[64:79]
	global_load_dwordx4 v[116:119], v64, s[4:5] offset:1152
	global_load_dwordx4 v[120:123], v66, s[4:5] offset:1152
	ds_read_b128 v[32:35], v84 offset:7168
	v_mfma_f32_32x32x16_f16 a[48:63], v[36:39], v[112:115], a[48:63]
	s_add_u32 m0, s47, 0x103c0
	s_add_u32 s42, s42, 0x1800
	s_addc_u32 s43, s43, 0
	global_load_lds_dwordx4 v77, s[42:43]
	ds_read_b128 v[36:39], v84 offset:8192
	v_mfma_f32_32x32x16_f16 a[32:47], v[40:43], v[112:115], a[32:47]
	global_load_dwordx4 v[124:127], v68, s[4:5] offset:1152
	global_load_dwordx4 v[128:131], v70, s[4:5] offset:1152
	ds_read_b128 v[40:43], v84 offset:9216
	v_mfma_f32_32x32x16_f16 a[16:31], v[44:47], v[112:115], a[16:31]
	s_add_u32 m0, s48, 0x103c0
	s_add_u32 s44, s44, 0x1800
	s_addc_u32 s45, s45, 0
	global_load_lds_dwordx4 v78, s[44:45]
	ds_read_b128 v[44:47], v84 offset:10240
	v_mfma_f32_32x32x16_f16 a[0:15], v[48:51], v[112:115], a[0:15]
	ds_read_b128 v[48:51], v84 offset:11264
	s_waitcnt lgkmcnt(6)
	v_mfma_f32_32x32x16_f16 a[80:95], v[4:7], v[52:55], a[80:95]
	v_mfma_f32_32x32x16_f16 a[64:79], v[8:11], v[52:55], a[64:79]
	v_mfma_f32_32x32x16_f16 a[48:63], v[12:15], v[52:55], a[48:63]
	s_waitcnt vmcnt(10)
	s_waitcnt lgkmcnt(0)
	s_barrier
	ds_read_b128 v[4:7], v84 offset:12288
	ds_read_b128 v[8:11], v84 offset:13312
	ds_read_b128 v[12:15], v84 offset:14336
	v_mfma_f32_32x32x16_f16 a[32:47], v[16:19], v[52:55], a[32:47]
	ds_read_b128 v[16:19], v84 offset:15360
	v_mfma_f32_32x32x16_f16 a[16:31], v[20:23], v[52:55], a[16:31]
	ds_read_b128 v[20:23], v84 offset:16384
	v_mfma_f32_32x32x16_f16 a[0:15], v[24:27], v[52:55], a[0:15]
	ds_read_b128 v[24:27], v84 offset:17408
	v_mfma_f32_32x32x16_f16 a[80:95], v[28:31], v[56:59], a[80:95]
	s_add_u32 m0, s46, 0x0
	s_add_u32 s40, s40, 0x1800
	s_addc_u32 s41, s41, 0
	global_load_lds_dwordx4 v76, s[40:41]
	ds_read_b128 v[28:31], v84 offset:18432
	v_mfma_f32_32x32x16_f16 a[64:79], v[32:35], v[56:59], a[64:79]
	ds_read_b128 v[32:35], v84 offset:19456
	v_mfma_f32_32x32x16_f16 a[48:63], v[36:39], v[56:59], a[48:63]
	s_add_u32 m0, s47, 0x0
	s_add_u32 s42, s42, 0x1800
	s_addc_u32 s43, s43, 0
	global_load_lds_dwordx4 v77, s[42:43]
	ds_read_b128 v[36:39], v84 offset:20480
	v_mfma_f32_32x32x16_f16 a[32:47], v[40:43], v[56:59], a[32:47]
	ds_read_b128 v[40:43], v84 offset:21504
	v_mfma_f32_32x32x16_f16 a[16:31], v[44:47], v[56:59], a[16:31]
	s_add_u32 m0, s48, 0x0
	s_add_u32 s44, s44, 0x1800
	s_addc_u32 s45, s45, 0
	global_load_lds_dwordx4 v78, s[44:45]
	ds_read_b128 v[44:47], v84 offset:22528
	v_mfma_f32_32x32x16_f16 a[0:15], v[48:51], v[56:59], a[0:15]
	ds_read_b128 v[48:51], v84 offset:23552
	s_waitcnt lgkmcnt(6)
	v_mfma_f32_32x32x16_f16 a[80:95], v[4:7], v[60:63], a[80:95]
	s_waitcnt vmcnt(24)
	ds_write_b128 v81, v[132:135]
	ds_write_b128 v81, v[136:139] offset:1024
	v_mfma_f32_32x32x16_f16 a[64:79], v[8:11], v[60:63], a[64:79]
	ds_write_b128 v81, v[140:143] offset:2048
	ds_write_b128 v81, v[144:147] offset:3072
	v_mfma_f32_32x32x16_f16 a[48:63], v[12:15], v[60:63], a[48:63]
	ds_read_b128 v[100:103], v95
	ds_read_b128 v[104:107], v96
	ds_read_b128 v[108:111], v97
	ds_read_b128 v[112:115], v94
	s_waitcnt vmcnt(10)
	s_waitcnt lgkmcnt(8)
	s_barrier
	ds_read_b128 v[4:7], v84 offset:54208
	ds_read_b128 v[8:11], v84 offset:55232
	ds_read_b128 v[12:15], v84 offset:56256
	v_mfma_f32_32x32x16_f16 a[32:47], v[16:19], v[60:63], a[32:47]
	ds_read_b128 v[16:19], v84 offset:57280
	v_mfma_f32_32x32x16_f16 a[16:31], v[20:23], v[60:63], a[16:31]
	ds_read_b128 v[20:23], v84 offset:58304
	v_mfma_f32_32x32x16_f16 a[0:15], v[24:27], v[60:63], a[0:15]
	ds_read_b128 v[24:27], v84 offset:59328
	s_waitcnt lgkmcnt(6)
	v_mfma_f32_32x32x16_f16 a[80:95], v[28:31], v[0:3], a[80:95]
	s_add_u32 m0, s46, 0x3000
	s_add_u32 s40, s40, 0x1800
	s_addc_u32 s41, s41, 0
	global_load_lds_dwordx4 v76, s[40:41]
	ds_read_b128 v[28:31], v84 offset:60352
	v_mfma_f32_32x32x16_f16 a[64:79], v[32:35], v[0:3], a[64:79]
	global_load_dwordx4 v[132:135], v64, s[4:5] offset:1280
	global_load_dwordx4 v[136:139], v66, s[4:5] offset:1280
	ds_read_b128 v[32:35], v84 offset:61376
	v_mfma_f32_32x32x16_f16 a[48:63], v[36:39], v[0:3], a[48:63]
	s_add_u32 m0, s47, 0x3000
	s_add_u32 s42, s42, 0x1800
	s_addc_u32 s43, s43, 0
	global_load_lds_dwordx4 v77, s[42:43]
	ds_read_b128 v[36:39], v84 offset:62400
	v_mfma_f32_32x32x16_f16 a[32:47], v[40:43], v[0:3], a[32:47]
	global_load_dwordx4 v[140:143], v68, s[4:5] offset:1280
	global_load_dwordx4 v[144:147], v70, s[4:5] offset:1280
	ds_read_b128 v[40:43], v84 offset:63424
	v_mfma_f32_32x32x16_f16 a[16:31], v[44:47], v[0:3], a[16:31]
	s_add_u32 m0, s48, 0x3000
	s_add_u32 s44, s44, 0x1800
	s_addc_u32 s45, s45, 0
	global_load_lds_dwordx4 v78, s[44:45]
	ds_read_b128 v[44:47], v84 offset:64448
	v_mfma_f32_32x32x16_f16 a[0:15], v[48:51], v[0:3], a[0:15]
	ds_read_b128 v[48:51], v84 offset:65472
	s_waitcnt lgkmcnt(6)
	v_mfma_f32_32x32x16_f16 a[80:95], v[4:7], v[100:103], a[80:95]
	v_mfma_f32_32x32x16_f16 a[64:79], v[8:11], v[100:103], a[64:79]
	v_mfma_f32_32x32x16_f16 a[48:63], v[12:15], v[100:103], a[48:63]
	s_waitcnt vmcnt(10)
	s_waitcnt lgkmcnt(0)
	s_barrier
	ds_read_b128 v[4:7], v98
	ds_read_b128 v[8:11], v98 offset:1024
	ds_read_b128 v[12:15], v98 offset:2048
	v_mfma_f32_32x32x16_f16 a[32:47], v[16:19], v[100:103], a[32:47]
	ds_read_b128 v[16:19], v98 offset:3072
	v_mfma_f32_32x32x16_f16 a[16:31], v[20:23], v[100:103], a[16:31]
	ds_read_b128 v[20:23], v98 offset:4096
	v_mfma_f32_32x32x16_f16 a[0:15], v[24:27], v[100:103], a[0:15]
	ds_read_b128 v[24:27], v98 offset:5120
	v_mfma_f32_32x32x16_f16 a[80:95], v[28:31], v[104:107], a[80:95]
	s_add_u32 m0, s46, 0xd3c0
	s_add_u32 s40, s40, 0x1800
	s_addc_u32 s41, s41, 0
	global_load_lds_dwordx4 v76, s[40:41]
	ds_read_b128 v[28:31], v98 offset:6144
	v_mfma_f32_32x32x16_f16 a[64:79], v[32:35], v[104:107], a[64:79]
	ds_read_b128 v[32:35], v98 offset:7168
	v_mfma_f32_32x32x16_f16 a[48:63], v[36:39], v[104:107], a[48:63]
	s_add_u32 m0, s47, 0xd3c0
	s_add_u32 s42, s42, 0x1800
	s_addc_u32 s43, s43, 0
	global_load_lds_dwordx4 v77, s[42:43]
	ds_read_b128 v[36:39], v98 offset:8192
	v_mfma_f32_32x32x16_f16 a[32:47], v[40:43], v[104:107], a[32:47]
	ds_read_b128 v[40:43], v98 offset:9216
	v_mfma_f32_32x32x16_f16 a[16:31], v[44:47], v[104:107], a[16:31]
	s_add_u32 m0, s48, 0xd3c0
	s_add_u32 s44, s44, 0x1800
	s_addc_u32 s45, s45, 0
	global_load_lds_dwordx4 v78, s[44:45]
	ds_read_b128 v[44:47], v98 offset:10240
	v_mfma_f32_32x32x16_f16 a[0:15], v[48:51], v[104:107], a[0:15]
	ds_read_b128 v[48:51], v98 offset:11264
	s_waitcnt lgkmcnt(6)
	v_mfma_f32_32x32x16_f16 a[80:95], v[4:7], v[108:111], a[80:95]
	s_waitcnt vmcnt(24)
	ds_write_b128 v81, v[148:151]
	ds_write_b128 v81, v[152:155] offset:1024
	v_mfma_f32_32x32x16_f16 a[64:79], v[8:11], v[108:111], a[64:79]
	ds_write_b128 v81, v[156:159] offset:2048
	ds_write_b128 v81, v[72:75] offset:3072
	v_mfma_f32_32x32x16_f16 a[48:63], v[12:15], v[108:111], a[48:63]
	ds_read_b128 v[52:55], v95
	ds_read_b128 v[56:59], v96
	ds_read_b128 v[60:63], v97
	ds_read_b128 v[0:3], v94
	s_waitcnt vmcnt(10)
	s_waitcnt lgkmcnt(8)
	s_barrier
	ds_read_b128 v[4:7], v84 offset:0
	ds_read_b128 v[8:11], v84 offset:1024
	ds_read_b128 v[12:15], v84 offset:2048
	v_mfma_f32_32x32x16_f16 a[32:47], v[16:19], v[108:111], a[32:47]
	ds_read_b128 v[16:19], v84 offset:3072
	v_mfma_f32_32x32x16_f16 a[16:31], v[20:23], v[108:111], a[16:31]
	ds_read_b128 v[20:23], v84 offset:4096
	v_mfma_f32_32x32x16_f16 a[0:15], v[24:27], v[108:111], a[0:15]
	ds_read_b128 v[24:27], v84 offset:5120
	s_waitcnt lgkmcnt(6)
	v_mfma_f32_32x32x16_f16 a[80:95], v[28:31], v[112:115], a[80:95]
	s_add_u32 m0, s46, 0x103c0
	s_add_u32 s40, s40, 0x1800
	s_addc_u32 s41, s41, 0
	global_load_lds_dwordx4 v76, s[40:41]
	ds_read_b128 v[28:31], v84 offset:6144
	v_mfma_f32_32x32x16_f16 a[64:79], v[32:35], v[112:115], a[64:79]
	global_load_dwordx4 v[148:151], v64, s[4:5] offset:1408
	global_load_dwordx4 v[152:155], v66, s[4:5] offset:1408
	ds_read_b128 v[32:35], v84 offset:7168
	v_mfma_f32_32x32x16_f16 a[48:63], v[36:39], v[112:115], a[48:63]
	s_add_u32 m0, s47, 0x103c0
	s_add_u32 s42, s42, 0x1800
	s_addc_u32 s43, s43, 0
	global_load_lds_dwordx4 v77, s[42:43]
	ds_read_b128 v[36:39], v84 offset:8192
	v_mfma_f32_32x32x16_f16 a[32:47], v[40:43], v[112:115], a[32:47]
	global_load_dwordx4 v[156:159], v68, s[4:5] offset:1408
	global_load_dwordx4 v[72:75], v70, s[4:5] offset:1408
	ds_read_b128 v[40:43], v84 offset:9216
	v_mfma_f32_32x32x16_f16 a[16:31], v[44:47], v[112:115], a[16:31]
	s_add_u32 m0, s48, 0x103c0
	s_add_u32 s44, s44, 0x1800
	s_addc_u32 s45, s45, 0
	global_load_lds_dwordx4 v78, s[44:45]
	ds_read_b128 v[44:47], v84 offset:10240
	v_mfma_f32_32x32x16_f16 a[0:15], v[48:51], v[112:115], a[0:15]
	ds_read_b128 v[48:51], v84 offset:11264
	s_waitcnt lgkmcnt(6)
	v_mfma_f32_32x32x16_f16 a[80:95], v[4:7], v[52:55], a[80:95]
	v_mfma_f32_32x32x16_f16 a[64:79], v[8:11], v[52:55], a[64:79]
	v_mfma_f32_32x32x16_f16 a[48:63], v[12:15], v[52:55], a[48:63]
	s_waitcnt vmcnt(10)
	s_waitcnt lgkmcnt(0)
	s_barrier
	ds_read_b128 v[4:7], v84 offset:12288
	ds_read_b128 v[8:11], v84 offset:13312
	ds_read_b128 v[12:15], v84 offset:14336
	v_mfma_f32_32x32x16_f16 a[32:47], v[16:19], v[52:55], a[32:47]
	ds_read_b128 v[16:19], v84 offset:15360
	v_mfma_f32_32x32x16_f16 a[16:31], v[20:23], v[52:55], a[16:31]
	ds_read_b128 v[20:23], v84 offset:16384
	v_mfma_f32_32x32x16_f16 a[0:15], v[24:27], v[52:55], a[0:15]
	ds_read_b128 v[24:27], v84 offset:17408
	v_mfma_f32_32x32x16_f16 a[80:95], v[28:31], v[56:59], a[80:95]
	s_add_u32 m0, s46, 0x0
	s_add_u32 s40, s40, 0x1800
	s_addc_u32 s41, s41, 0
	global_load_lds_dwordx4 v76, s[40:41]
	ds_read_b128 v[28:31], v84 offset:18432
	v_mfma_f32_32x32x16_f16 a[64:79], v[32:35], v[56:59], a[64:79]
	ds_read_b128 v[32:35], v84 offset:19456
	v_mfma_f32_32x32x16_f16 a[48:63], v[36:39], v[56:59], a[48:63]
	s_add_u32 m0, s47, 0x0
	s_add_u32 s42, s42, 0x1800
	s_addc_u32 s43, s43, 0
	global_load_lds_dwordx4 v77, s[42:43]
	ds_read_b128 v[36:39], v84 offset:20480
	v_mfma_f32_32x32x16_f16 a[32:47], v[40:43], v[56:59], a[32:47]
	ds_read_b128 v[40:43], v84 offset:21504
	v_mfma_f32_32x32x16_f16 a[16:31], v[44:47], v[56:59], a[16:31]
	s_add_u32 m0, s48, 0x0
	s_add_u32 s44, s44, 0x1800
	s_addc_u32 s45, s45, 0
	global_load_lds_dwordx4 v78, s[44:45]
	ds_read_b128 v[44:47], v84 offset:22528
	v_mfma_f32_32x32x16_f16 a[0:15], v[48:51], v[56:59], a[0:15]
	ds_read_b128 v[48:51], v84 offset:23552
	s_waitcnt lgkmcnt(6)
	v_mfma_f32_32x32x16_f16 a[80:95], v[4:7], v[60:63], a[80:95]
	s_waitcnt vmcnt(24)
	ds_write_b128 v81, v[116:119]
	ds_write_b128 v81, v[120:123] offset:1024
	v_mfma_f32_32x32x16_f16 a[64:79], v[8:11], v[60:63], a[64:79]
	ds_write_b128 v81, v[124:127] offset:2048
	ds_write_b128 v81, v[128:131] offset:3072
	v_mfma_f32_32x32x16_f16 a[48:63], v[12:15], v[60:63], a[48:63]
	ds_read_b128 v[100:103], v95
	ds_read_b128 v[104:107], v96
	ds_read_b128 v[108:111], v97
	ds_read_b128 v[112:115], v94
	s_waitcnt vmcnt(10)
	s_waitcnt lgkmcnt(8)
	s_barrier
	ds_read_b128 v[4:7], v84 offset:54208
	ds_read_b128 v[8:11], v84 offset:55232
	ds_read_b128 v[12:15], v84 offset:56256
	v_mfma_f32_32x32x16_f16 a[32:47], v[16:19], v[60:63], a[32:47]
	ds_read_b128 v[16:19], v84 offset:57280
	v_mfma_f32_32x32x16_f16 a[16:31], v[20:23], v[60:63], a[16:31]
	ds_read_b128 v[20:23], v84 offset:58304
	v_mfma_f32_32x32x16_f16 a[0:15], v[24:27], v[60:63], a[0:15]
	ds_read_b128 v[24:27], v84 offset:59328
	s_waitcnt lgkmcnt(6)
	v_mfma_f32_32x32x16_f16 a[80:95], v[28:31], v[0:3], a[80:95]
	s_add_u32 m0, s46, 0x3000
	s_add_u32 s40, s40, 0x1800
	s_addc_u32 s41, s41, 0
	global_load_lds_dwordx4 v76, s[40:41]
	ds_read_b128 v[28:31], v84 offset:60352
	v_mfma_f32_32x32x16_f16 a[64:79], v[32:35], v[0:3], a[64:79]
	global_load_dwordx4 v[116:119], v64, s[4:5] offset:1440
	global_load_dwordx4 v[120:123], v66, s[4:5] offset:1440
	ds_read_b128 v[32:35], v84 offset:61376
	v_mfma_f32_32x32x16_f16 a[48:63], v[36:39], v[0:3], a[48:63]
	s_add_u32 m0, s47, 0x3000
	s_add_u32 s42, s42, 0x1800
	s_addc_u32 s43, s43, 0
	global_load_lds_dwordx4 v77, s[42:43]
	ds_read_b128 v[36:39], v84 offset:62400
	v_mfma_f32_32x32x16_f16 a[32:47], v[40:43], v[0:3], a[32:47]
	global_load_dwordx4 v[124:127], v68, s[4:5] offset:1440
	global_load_dwordx4 v[128:131], v70, s[4:5] offset:1440
	ds_read_b128 v[40:43], v84 offset:63424
	v_mfma_f32_32x32x16_f16 a[16:31], v[44:47], v[0:3], a[16:31]
	s_add_u32 m0, s48, 0x3000
	s_add_u32 s44, s44, 0x1800
	s_addc_u32 s45, s45, 0
	global_load_lds_dwordx4 v78, s[44:45]
	ds_read_b128 v[44:47], v84 offset:64448
	v_mfma_f32_32x32x16_f16 a[0:15], v[48:51], v[0:3], a[0:15]
	ds_read_b128 v[48:51], v84 offset:65472
	s_waitcnt lgkmcnt(6)
	v_mfma_f32_32x32x16_f16 a[80:95], v[4:7], v[100:103], a[80:95]
	v_mfma_f32_32x32x16_f16 a[64:79], v[8:11], v[100:103], a[64:79]
	v_mfma_f32_32x32x16_f16 a[48:63], v[12:15], v[100:103], a[48:63]
	s_waitcnt vmcnt(10)
	s_waitcnt lgkmcnt(0)
	s_barrier
	ds_read_b128 v[4:7], v98
	ds_read_b128 v[8:11], v98 offset:1024
	ds_read_b128 v[12:15], v98 offset:2048
	v_mfma_f32_32x32x16_f16 a[32:47], v[16:19], v[100:103], a[32:47]
	ds_read_b128 v[16:19], v98 offset:3072
	v_mfma_f32_32x32x16_f16 a[16:31], v[20:23], v[100:103], a[16:31]
	ds_read_b128 v[20:23], v98 offset:4096
	v_mfma_f32_32x32x16_f16 a[0:15], v[24:27], v[100:103], a[0:15]
	ds_read_b128 v[24:27], v98 offset:5120
	v_mfma_f32_32x32x16_f16 a[80:95], v[28:31], v[104:107], a[80:95]
	s_add_u32 m0, s46, 0xd3c0
	s_add_u32 s40, s40, 0x1800
	s_addc_u32 s41, s41, 0
	global_load_lds_dwordx4 v76, s[40:41]
	ds_read_b128 v[28:31], v98 offset:6144
	v_mfma_f32_32x32x16_f16 a[64:79], v[32:35], v[104:107], a[64:79]
	ds_read_b128 v[32:35], v98 offset:7168
	v_mfma_f32_32x32x16_f16 a[48:63], v[36:39], v[104:107], a[48:63]
	s_add_u32 m0, s47, 0xd3c0
	s_add_u32 s42, s42, 0x1800
	s_addc_u32 s43, s43, 0
	global_load_lds_dwordx4 v77, s[42:43]
	ds_read_b128 v[36:39], v98 offset:8192
	v_mfma_f32_32x32x16_f16 a[32:47], v[40:43], v[104:107], a[32:47]
	ds_read_b128 v[40:43], v98 offset:9216
	v_mfma_f32_32x32x16_f16 a[16:31], v[44:47], v[104:107], a[16:31]
	s_add_u32 m0, s48, 0xd3c0
	s_add_u32 s44, s44, 0x1800
	s_addc_u32 s45, s45, 0
	global_load_lds_dwordx4 v78, s[44:45]
	ds_read_b128 v[44:47], v98 offset:10240
	v_mfma_f32_32x32x16_f16 a[0:15], v[48:51], v[104:107], a[0:15]
	ds_read_b128 v[48:51], v98 offset:11264
	s_waitcnt lgkmcnt(6)
	v_mfma_f32_32x32x16_f16 a[80:95], v[4:7], v[108:111], a[80:95]
	s_waitcnt vmcnt(24)
	ds_write_b128 v81, v[132:135]
	ds_write_b128 v81, v[136:139] offset:1024
	v_mfma_f32_32x32x16_f16 a[64:79], v[8:11], v[108:111], a[64:79]
	ds_write_b128 v81, v[140:143] offset:2048
	ds_write_b128 v81, v[144:147] offset:3072
	v_mfma_f32_32x32x16_f16 a[48:63], v[12:15], v[108:111], a[48:63]
	ds_read_b128 v[52:55], v95
	ds_read_b128 v[56:59], v96
	ds_read_b128 v[60:63], v97
	ds_read_b128 v[0:3], v94
	s_waitcnt vmcnt(10)
	s_waitcnt lgkmcnt(8)
	s_barrier
	ds_read_b128 v[4:7], v84 offset:0
	ds_read_b128 v[8:11], v84 offset:1024
	ds_read_b128 v[12:15], v84 offset:2048
	v_mfma_f32_32x32x16_f16 a[32:47], v[16:19], v[108:111], a[32:47]
	ds_read_b128 v[16:19], v84 offset:3072
	v_mfma_f32_32x32x16_f16 a[16:31], v[20:23], v[108:111], a[16:31]
	ds_read_b128 v[20:23], v84 offset:4096
	v_mfma_f32_32x32x16_f16 a[0:15], v[24:27], v[108:111], a[0:15]
	ds_read_b128 v[24:27], v84 offset:5120
	s_waitcnt lgkmcnt(6)
	v_mfma_f32_32x32x16_f16 a[80:95], v[28:31], v[112:115], a[80:95]
	s_add_u32 m0, s46, 0x103c0
	s_add_u32 s40, s40, 0x1800
	s_addc_u32 s41, s41, 0
	global_load_lds_dwordx4 v76, s[40:41]
	ds_read_b128 v[28:31], v84 offset:6144
	v_mfma_f32_32x32x16_f16 a[64:79], v[32:35], v[112:115], a[64:79]
	ds_read_b128 v[32:35], v84 offset:7168
	v_mfma_f32_32x32x16_f16 a[48:63], v[36:39], v[112:115], a[48:63]
	s_add_u32 m0, s47, 0x103c0
	s_add_u32 s42, s42, 0x1800
	s_addc_u32 s43, s43, 0
	global_load_lds_dwordx4 v77, s[42:43]
	ds_read_b128 v[36:39], v84 offset:8192
	v_mfma_f32_32x32x16_f16 a[32:47], v[40:43], v[112:115], a[32:47]
	ds_read_b128 v[40:43], v84 offset:9216
	v_mfma_f32_32x32x16_f16 a[16:31], v[44:47], v[112:115], a[16:31]
	s_add_u32 m0, s48, 0x103c0
	s_add_u32 s44, s44, 0x1800
	s_addc_u32 s45, s45, 0
	global_load_lds_dwordx4 v78, s[44:45]
	ds_read_b128 v[44:47], v84 offset:10240
	v_mfma_f32_32x32x16_f16 a[0:15], v[48:51], v[112:115], a[0:15]
	ds_read_b128 v[48:51], v84 offset:11264
	s_waitcnt lgkmcnt(6)
	v_mfma_f32_32x32x16_f16 a[80:95], v[4:7], v[52:55], a[80:95]
	v_mfma_f32_32x32x16_f16 a[64:79], v[8:11], v[52:55], a[64:79]
	v_mfma_f32_32x32x16_f16 a[48:63], v[12:15], v[52:55], a[48:63]
	s_waitcnt vmcnt(6)
	s_waitcnt lgkmcnt(0)
	s_barrier
	ds_read_b128 v[4:7], v84 offset:12288
	ds_read_b128 v[8:11], v84 offset:13312
	ds_read_b128 v[12:15], v84 offset:14336
	v_mfma_f32_32x32x16_f16 a[32:47], v[16:19], v[52:55], a[32:47]
	ds_read_b128 v[16:19], v84 offset:15360
	v_mfma_f32_32x32x16_f16 a[16:31], v[20:23], v[52:55], a[16:31]
	ds_read_b128 v[20:23], v84 offset:16384
	v_mfma_f32_32x32x16_f16 a[0:15], v[24:27], v[52:55], a[0:15]
	ds_read_b128 v[24:27], v84 offset:17408
	v_mfma_f32_32x32x16_f16 a[80:95], v[28:31], v[56:59], a[80:95]
	s_add_u32 m0, s46, 0x0
	s_add_u32 s40, s40, 0x1800
	s_addc_u32 s41, s41, 0
	global_load_lds_dwordx4 v76, s[40:41]
	ds_read_b128 v[28:31], v84 offset:18432
	v_mfma_f32_32x32x16_f16 a[64:79], v[32:35], v[56:59], a[64:79]
	ds_read_b128 v[32:35], v84 offset:19456
	v_mfma_f32_32x32x16_f16 a[48:63], v[36:39], v[56:59], a[48:63]
	s_add_u32 m0, s47, 0x0
	s_add_u32 s42, s42, s49
	s_addc_u32 s43, s43, 0
	global_load_lds_dwordx4 v77, s[42:43]
	ds_read_b128 v[36:39], v84 offset:20480
	v_mfma_f32_32x32x16_f16 a[32:47], v[40:43], v[56:59], a[32:47]
	ds_read_b128 v[40:43], v84 offset:21504
	v_mfma_f32_32x32x16_f16 a[16:31], v[44:47], v[56:59], a[16:31]
	ds_read_b128 v[44:47], v84 offset:22528
	v_mfma_f32_32x32x16_f16 a[0:15], v[48:51], v[56:59], a[0:15]
	ds_read_b128 v[48:51], v84 offset:23552
	s_waitcnt lgkmcnt(6)
	v_mfma_f32_32x32x16_f16 a[80:95], v[4:7], v[60:63], a[80:95]
	s_waitcnt vmcnt(19)
	ds_write_b128 v81, v[148:151]
	ds_write_b128 v81, v[152:155] offset:1024
	v_mfma_f32_32x32x16_f16 a[64:79], v[8:11], v[60:63], a[64:79]
	ds_write_b128 v81, v[156:159] offset:2048
	ds_write_b128 v81, v[72:75] offset:3072
	v_mfma_f32_32x32x16_f16 a[48:63], v[12:15], v[60:63], a[48:63]
	ds_read_b128 v[100:103], v95
	ds_read_b128 v[104:107], v96
	ds_read_b128 v[108:111], v97
	ds_read_b128 v[112:115], v94
	s_waitcnt vmcnt(5)
	s_waitcnt lgkmcnt(8)
	s_barrier
	ds_read_b128 v[4:7], v84 offset:54208
	ds_read_b128 v[8:11], v84 offset:55232
	ds_read_b128 v[12:15], v84 offset:56256
	v_mfma_f32_32x32x16_f16 a[32:47], v[16:19], v[60:63], a[32:47]
	ds_read_b128 v[16:19], v84 offset:57280
	v_mfma_f32_32x32x16_f16 a[16:31], v[20:23], v[60:63], a[16:31]
	ds_read_b128 v[20:23], v84 offset:58304
	v_mfma_f32_32x32x16_f16 a[0:15], v[24:27], v[60:63], a[0:15]
	ds_read_b128 v[24:27], v84 offset:59328
	s_waitcnt lgkmcnt(6)
	v_mfma_f32_32x32x16_f16 a[80:95], v[28:31], v[0:3], a[80:95]
	ds_read_b128 v[28:31], v84 offset:60352
	v_mfma_f32_32x32x16_f16 a[64:79], v[32:35], v[0:3], a[64:79]
	ds_read_b128 v[32:35], v84 offset:61376
	v_mfma_f32_32x32x16_f16 a[48:63], v[36:39], v[0:3], a[48:63]
	ds_read_b128 v[36:39], v84 offset:62400
	v_mfma_f32_32x32x16_f16 a[32:47], v[40:43], v[0:3], a[32:47]
	ds_read_b128 v[40:43], v84 offset:63424
	v_mfma_f32_32x32x16_f16 a[16:31], v[44:47], v[0:3], a[16:31]
	ds_read_b128 v[44:47], v84 offset:64448
	v_mfma_f32_32x32x16_f16 a[0:15], v[48:51], v[0:3], a[0:15]
	ds_read_b128 v[48:51], v84 offset:65472
	s_waitcnt lgkmcnt(6)
	v_mfma_f32_32x32x16_f16 a[80:95], v[4:7], v[100:103], a[80:95]
	v_mfma_f32_32x32x16_f16 a[64:79], v[8:11], v[100:103], a[64:79]
	v_mfma_f32_32x32x16_f16 a[48:63], v[12:15], v[100:103], a[48:63]
	s_waitcnt vmcnt(2)
	s_waitcnt lgkmcnt(0)
	s_barrier
	ds_read_b128 v[4:7], v98
	ds_read_b128 v[8:11], v98 offset:1024
	ds_read_b128 v[12:15], v98 offset:2048
	v_mfma_f32_32x32x16_f16 a[32:47], v[16:19], v[100:103], a[32:47]
	ds_read_b128 v[16:19], v98 offset:3072
	v_mfma_f32_32x32x16_f16 a[16:31], v[20:23], v[100:103], a[16:31]
	ds_read_b128 v[20:23], v98 offset:4096
	v_mfma_f32_32x32x16_f16 a[0:15], v[24:27], v[100:103], a[0:15]
	ds_read_b128 v[24:27], v98 offset:5120
	v_mfma_f32_32x32x16_f16 a[80:95], v[28:31], v[104:107], a[80:95]
	ds_read_b128 v[28:31], v98 offset:6144
	v_mfma_f32_32x32x16_f16 a[64:79], v[32:35], v[104:107], a[64:79]
	ds_read_b128 v[32:35], v98 offset:7168
	v_mfma_f32_32x32x16_f16 a[48:63], v[36:39], v[104:107], a[48:63]
	ds_read_b128 v[36:39], v98 offset:8192
	v_mfma_f32_32x32x16_f16 a[32:47], v[40:43], v[104:107], a[32:47]
	ds_read_b128 v[40:43], v98 offset:9216
	v_mfma_f32_32x32x16_f16 a[16:31], v[44:47], v[104:107], a[16:31]
	ds_read_b128 v[44:47], v98 offset:10240
	v_mfma_f32_32x32x16_f16 a[0:15], v[48:51], v[104:107], a[0:15]
	ds_read_b128 v[48:51], v98 offset:11264
	s_waitcnt lgkmcnt(6)
	v_mfma_f32_32x32x16_f16 a[80:95], v[4:7], v[108:111], a[80:95]
	s_waitcnt vmcnt(9)
	ds_write_b128 v81, v[116:119]
	ds_write_b128 v81, v[120:123] offset:1024
	v_mfma_f32_32x32x16_f16 a[64:79], v[8:11], v[108:111], a[64:79]
	ds_write_b128 v81, v[124:127] offset:2048
	ds_write_b128 v81, v[128:131] offset:3072
	v_mfma_f32_32x32x16_f16 a[48:63], v[12:15], v[108:111], a[48:63]
	ds_read_b128 v[0:3], v94
	s_waitcnt vmcnt(0)
	s_waitcnt lgkmcnt(5)
	s_barrier
	ds_read_b128 v[4:7], v84 offset:0
	ds_read_b128 v[8:11], v84 offset:1024
	ds_read_b128 v[12:15], v84 offset:2048
	v_mfma_f32_32x32x16_f16 a[32:47], v[16:19], v[108:111], a[32:47]
	ds_read_b128 v[16:19], v84 offset:3072
	v_mfma_f32_32x32x16_f16 a[16:31], v[20:23], v[108:111], a[16:31]
	ds_read_b128 v[20:23], v84 offset:4096
	v_mfma_f32_32x32x16_f16 a[0:15], v[24:27], v[108:111], a[0:15]
	ds_read_b128 v[24:27], v84 offset:5120
	s_waitcnt lgkmcnt(6)
	v_mfma_f32_32x32x16_f16 a[80:95], v[28:31], v[112:115], a[80:95]
	v_mfma_f32_32x32x16_f16 a[64:79], v[32:35], v[112:115], a[64:79]
	v_mfma_f32_32x32x16_f16 a[48:63], v[36:39], v[112:115], a[48:63]
	v_mfma_f32_32x32x16_f16 a[32:47], v[40:43], v[112:115], a[32:47]
	v_mfma_f32_32x32x16_f16 a[16:31], v[44:47], v[112:115], a[16:31]
	v_mfma_f32_32x32x16_f16 a[0:15], v[48:51], v[112:115], a[0:15]
	s_waitcnt lgkmcnt(0)
	v_mfma_f32_32x32x16_f16 a[80:95], v[4:7], v[0:3], a[80:95]
	v_mfma_f32_32x32x16_f16 a[16:31], v[20:23], v[0:3], a[16:31]
	v_lshlrev_b32_e32 v22, 4, v85
	v_mfma_f32_32x32x16_f16 a[64:79], v[8:11], v[0:3], a[64:79]
	v_mfma_f32_32x32x16_f16 a[48:63], v[12:15], v[0:3], a[48:63]
	s_nop 7
	v_accvgpr_read_b32 v13, a88
	v_mfma_f32_32x32x16_f16 a[32:47], v[16:19], v[0:3], a[32:47]
	v_accvgpr_read_b32 v17, a92
	v_mfma_f32_32x32x16_f16 a[0:15], v[24:27], v[0:3], a[0:15]
	ds_read_b128 v[2:5], v22 offset:53248
	ds_read_b128 v[6:9], v22 offset:53280
	v_accvgpr_read_b32 v1, a80
	v_lshlrev_b32_e32 v0, 4, v92
	s_waitcnt lgkmcnt(1)
	v_add_f32_e32 v1, v1, v2
	v_accvgpr_read_b32 v2, a81
	v_add_f32_e32 v2, v3, v2
	v_max_f32_e32 v10, 0, v2
	v_accvgpr_read_b32 v2, a82
	v_add_f32_e32 v2, v4, v2
	v_max_f32_e32 v11, 0, v2
	v_accvgpr_read_b32 v2, a83
	v_add_f32_e32 v2, v5, v2
	v_max_f32_e32 v12, 0, v2
	v_accvgpr_read_b32 v2, a84
	s_waitcnt lgkmcnt(0)
	v_add_f32_e32 v2, v2, v6
	v_max_f32_e32 v6, 0, v2
	v_accvgpr_read_b32 v2, a85
	v_add_f32_e32 v2, v7, v2
	v_max_f32_e32 v7, 0, v2
	v_accvgpr_read_b32 v2, a86
	v_add_f32_e32 v2, v8, v2
	v_max_f32_e32 v8, 0, v2
	v_accvgpr_read_b32 v2, a87
	v_add_f32_e32 v2, v9, v2
	v_max_f32_e32 v9, 0, v2
	ds_read_b128 v[2:5], v22 offset:53312
	v_max_f32_e32 v1, 0, v1
	s_waitcnt lgkmcnt(0)
	v_add_f32_e32 v2, v13, v2
	v_max_f32_e32 v13, 0, v2
	v_accvgpr_read_b32 v2, a89
	v_add_f32_e32 v2, v3, v2
	v_max_f32_e32 v14, 0, v2
	v_accvgpr_read_b32 v2, a90
	v_add_f32_e32 v2, v4, v2
	v_max_f32_e32 v15, 0, v2
	v_accvgpr_read_b32 v2, a91
	v_add_f32_e32 v2, v5, v2
	v_max_f32_e32 v16, 0, v2
	ds_read_b128 v[2:5], v22 offset:53344
	s_waitcnt lgkmcnt(0)
	v_add_f32_e32 v2, v17, v2
	v_max_f32_e32 v17, 0, v2
	v_accvgpr_read_b32 v2, a93
	v_add_f32_e32 v2, v3, v2
	v_max_f32_e32 v18, 0, v2
	v_accvgpr_read_b32 v2, a94
	v_add_f32_e32 v2, v4, v2
	v_max_f32_e32 v19, 0, v2
	v_accvgpr_read_b32 v2, a95
	v_add_f32_e32 v2, v5, v2
	v_cvt_pk_f16_f32 v5, v8, v9
	v_cvt_pk_f16_f32 v4, v6, v7
	ds_read_b128 v[6:9], v0 offset:40960
	v_max_f32_e32 v20, 0, v2
	v_cvt_pk_f16_f32 v3, v11, v12
	v_cvt_pk_f16_f32 v2, v1, v10
	v_accvgpr_read_b32 v1, a64
	s_waitcnt lgkmcnt(0)
	v_mfma_f32_32x32x16_f16 a[80:95], v[6:9], v[2:5], 0
	ds_read_b128 v[6:9], v0 offset:41984
	v_cvt_pk_f16_f32 v5, v19, v20
	v_cvt_pk_f16_f32 v4, v17, v18
	v_cvt_pk_f16_f32 v3, v15, v16
	v_cvt_pk_f16_f32 v2, v13, v14
	v_accvgpr_read_b32 v13, a72
	v_accvgpr_read_b32 v17, a76
	s_waitcnt lgkmcnt(0)
	v_mfma_f32_32x32x16_f16 a[80:95], v[6:9], v[2:5], a[80:95]
	ds_read_b128 v[2:5], v22 offset:53376
	v_accvgpr_read_b32 v9, a68
	s_waitcnt lgkmcnt(0)
	v_add_f32_e32 v1, v1, v2
	v_accvgpr_read_b32 v2, a65
	v_add_f32_e32 v2, v3, v2
	v_max_f32_e32 v6, 0, v2
	v_accvgpr_read_b32 v2, a66
	v_add_f32_e32 v2, v4, v2
	v_max_f32_e32 v7, 0, v2
	v_accvgpr_read_b32 v2, a67
	v_add_f32_e32 v2, v5, v2
	v_max_f32_e32 v8, 0, v2
	ds_read_b128 v[2:5], v22 offset:53408
	v_max_f32_e32 v1, 0, v1
	s_waitcnt lgkmcnt(0)
	v_add_f32_e32 v2, v9, v2
	v_max_f32_e32 v9, 0, v2
	v_accvgpr_read_b32 v2, a69
	v_add_f32_e32 v2, v3, v2
	v_max_f32_e32 v10, 0, v2
	v_accvgpr_read_b32 v2, a70
	v_add_f32_e32 v2, v4, v2
	v_max_f32_e32 v11, 0, v2
	v_accvgpr_read_b32 v2, a71
	v_add_f32_e32 v2, v5, v2
	v_max_f32_e32 v12, 0, v2
	ds_read_b128 v[2:5], v22 offset:53440
	s_waitcnt lgkmcnt(0)
	v_add_f32_e32 v2, v13, v2
	v_max_f32_e32 v13, 0, v2
	v_accvgpr_read_b32 v2, a73
	v_add_f32_e32 v2, v3, v2
	v_max_f32_e32 v14, 0, v2
	v_accvgpr_read_b32 v2, a74
	v_add_f32_e32 v2, v4, v2
	v_max_f32_e32 v15, 0, v2
	v_accvgpr_read_b32 v2, a75
	v_add_f32_e32 v2, v5, v2
	v_max_f32_e32 v16, 0, v2
	ds_read_b128 v[2:5], v22 offset:53472
	s_waitcnt lgkmcnt(0)
	v_add_f32_e32 v2, v17, v2
	v_max_f32_e32 v17, 0, v2
	v_accvgpr_read_b32 v2, a77
	v_add_f32_e32 v2, v3, v2
	v_max_f32_e32 v18, 0, v2
	v_accvgpr_read_b32 v2, a78
	v_add_f32_e32 v2, v4, v2
	v_max_f32_e32 v19, 0, v2
	v_accvgpr_read_b32 v2, a79
	v_add_f32_e32 v2, v5, v2
	v_max_f32_e32 v20, 0, v2
	v_cvt_pk_f16_f32 v4, v9, v10
	v_cvt_pk_f16_f32 v3, v7, v8
	v_cvt_pk_f16_f32 v2, v1, v6
	ds_read_b128 v[6:9], v0 offset:43008
	v_cvt_pk_f16_f32 v5, v11, v12
	v_accvgpr_read_b32 v1, a48
	s_waitcnt lgkmcnt(0)
	v_mfma_f32_32x32x16_f16 a[80:95], v[6:9], v[2:5], a[80:95]
	ds_read_b128 v[6:9], v0 offset:44032
	v_cvt_pk_f16_f32 v5, v19, v20
	v_cvt_pk_f16_f32 v4, v17, v18
	v_cvt_pk_f16_f32 v3, v15, v16
	v_cvt_pk_f16_f32 v2, v13, v14
	v_accvgpr_read_b32 v13, a56
	v_accvgpr_read_b32 v17, a60
	s_waitcnt lgkmcnt(0)
	v_mfma_f32_32x32x16_f16 a[80:95], v[6:9], v[2:5], a[80:95]
	ds_read_b128 v[2:5], v22 offset:53504
	v_accvgpr_read_b32 v9, a52
	s_waitcnt lgkmcnt(0)
	v_add_f32_e32 v1, v1, v2
	v_accvgpr_read_b32 v2, a49
	v_add_f32_e32 v2, v3, v2
	v_max_f32_e32 v6, 0, v2
	v_accvgpr_read_b32 v2, a50
	v_add_f32_e32 v2, v4, v2
	v_max_f32_e32 v7, 0, v2
	v_accvgpr_read_b32 v2, a51
	v_add_f32_e32 v2, v5, v2
	v_max_f32_e32 v8, 0, v2
	ds_read_b128 v[2:5], v22 offset:53536
	v_max_f32_e32 v1, 0, v1
	s_waitcnt lgkmcnt(0)
	v_add_f32_e32 v2, v9, v2
	v_max_f32_e32 v9, 0, v2
	v_accvgpr_read_b32 v2, a53
	v_add_f32_e32 v2, v3, v2
	v_max_f32_e32 v10, 0, v2
	v_accvgpr_read_b32 v2, a54
	v_add_f32_e32 v2, v4, v2
	v_max_f32_e32 v11, 0, v2
	v_accvgpr_read_b32 v2, a55
	v_add_f32_e32 v2, v5, v2
	v_max_f32_e32 v12, 0, v2
	ds_read_b128 v[2:5], v22 offset:53568
	s_waitcnt lgkmcnt(0)
	v_add_f32_e32 v2, v13, v2
	v_max_f32_e32 v13, 0, v2
	v_accvgpr_read_b32 v2, a57
	v_add_f32_e32 v2, v3, v2
	v_max_f32_e32 v14, 0, v2
	v_accvgpr_read_b32 v2, a58
	v_add_f32_e32 v2, v4, v2
	v_max_f32_e32 v15, 0, v2
	v_accvgpr_read_b32 v2, a59
	v_add_f32_e32 v2, v5, v2
	v_max_f32_e32 v16, 0, v2
	ds_read_b128 v[2:5], v22 offset:53600
	s_waitcnt lgkmcnt(0)
	v_add_f32_e32 v2, v17, v2
	v_max_f32_e32 v17, 0, v2
	v_accvgpr_read_b32 v2, a61
	v_add_f32_e32 v2, v3, v2
	v_max_f32_e32 v18, 0, v2
	v_accvgpr_read_b32 v2, a62
	v_add_f32_e32 v2, v4, v2
	v_max_f32_e32 v19, 0, v2
	v_accvgpr_read_b32 v2, a63
	v_add_f32_e32 v2, v5, v2
	v_max_f32_e32 v20, 0, v2
	v_cvt_pk_f16_f32 v4, v9, v10
	v_cvt_pk_f16_f32 v3, v7, v8
	v_cvt_pk_f16_f32 v2, v1, v6
	ds_read_b128 v[6:9], v0 offset:45056
	v_cvt_pk_f16_f32 v5, v11, v12
	v_accvgpr_read_b32 v1, a32
	s_waitcnt lgkmcnt(0)
	v_mfma_f32_32x32x16_f16 a[80:95], v[6:9], v[2:5], a[80:95]
	ds_read_b128 v[6:9], v0 offset:46080
	v_cvt_pk_f16_f32 v5, v19, v20
	v_cvt_pk_f16_f32 v4, v17, v18
	v_cvt_pk_f16_f32 v3, v15, v16
	v_cvt_pk_f16_f32 v2, v13, v14
	v_accvgpr_read_b32 v13, a40
	v_accvgpr_read_b32 v17, a44
	s_waitcnt lgkmcnt(0)
	v_mfma_f32_32x32x16_f16 a[80:95], v[6:9], v[2:5], a[80:95]
	ds_read_b128 v[2:5], v22 offset:53632
	v_accvgpr_read_b32 v9, a36
	s_waitcnt lgkmcnt(0)
	v_add_f32_e32 v1, v1, v2
	v_accvgpr_read_b32 v2, a33
	v_add_f32_e32 v2, v3, v2
	v_max_f32_e32 v6, 0, v2
	v_accvgpr_read_b32 v2, a34
	v_add_f32_e32 v2, v4, v2
	v_max_f32_e32 v7, 0, v2
	v_accvgpr_read_b32 v2, a35
	v_add_f32_e32 v2, v5, v2
	v_max_f32_e32 v8, 0, v2
	ds_read_b128 v[2:5], v22 offset:53664
	v_max_f32_e32 v1, 0, v1
	s_waitcnt lgkmcnt(0)
	v_add_f32_e32 v2, v9, v2
	v_max_f32_e32 v9, 0, v2
	v_accvgpr_read_b32 v2, a37
	v_add_f32_e32 v2, v3, v2
	v_max_f32_e32 v10, 0, v2
	v_accvgpr_read_b32 v2, a38
	v_add_f32_e32 v2, v4, v2
	v_max_f32_e32 v11, 0, v2
	v_accvgpr_read_b32 v2, a39
	v_add_f32_e32 v2, v5, v2
	v_max_f32_e32 v12, 0, v2
	ds_read_b128 v[2:5], v22 offset:53696
	s_waitcnt lgkmcnt(0)
	v_add_f32_e32 v2, v13, v2
	v_max_f32_e32 v13, 0, v2
	v_accvgpr_read_b32 v2, a41
	v_add_f32_e32 v2, v3, v2
	v_max_f32_e32 v14, 0, v2
	v_accvgpr_read_b32 v2, a42
	v_add_f32_e32 v2, v4, v2
	v_max_f32_e32 v15, 0, v2
	v_accvgpr_read_b32 v2, a43
	v_add_f32_e32 v2, v5, v2
	v_max_f32_e32 v16, 0, v2
	ds_read_b128 v[2:5], v22 offset:53728
	s_waitcnt lgkmcnt(0)
	v_add_f32_e32 v2, v17, v2
	v_max_f32_e32 v17, 0, v2
	v_accvgpr_read_b32 v2, a45
	v_add_f32_e32 v2, v3, v2
	v_max_f32_e32 v18, 0, v2
	v_accvgpr_read_b32 v2, a46
	v_add_f32_e32 v2, v4, v2
	v_max_f32_e32 v19, 0, v2
	v_accvgpr_read_b32 v2, a47
	v_add_f32_e32 v2, v5, v2
	v_max_f32_e32 v20, 0, v2
	v_cvt_pk_f16_f32 v4, v9, v10
	v_cvt_pk_f16_f32 v3, v7, v8
	v_cvt_pk_f16_f32 v2, v1, v6
	ds_read_b128 v[6:9], v0 offset:47104
	v_cvt_pk_f16_f32 v5, v11, v12
	v_accvgpr_read_b32 v1, a16
	s_waitcnt lgkmcnt(0)
	v_mfma_f32_32x32x16_f16 a[32:47], v[6:9], v[2:5], 0
	ds_read_b128 v[6:9], v0 offset:48128
	v_cvt_pk_f16_f32 v5, v19, v20
	v_cvt_pk_f16_f32 v4, v17, v18
	v_cvt_pk_f16_f32 v3, v15, v16
	v_cvt_pk_f16_f32 v2, v13, v14
	v_accvgpr_read_b32 v13, a24
	v_accvgpr_read_b32 v17, a28
	s_waitcnt lgkmcnt(0)
	v_mfma_f32_32x32x16_f16 a[32:47], v[6:9], v[2:5], a[32:47]
	ds_read_b128 v[2:5], v22 offset:53760
	v_accvgpr_read_b32 v9, a20
	s_waitcnt lgkmcnt(0)
	v_add_f32_e32 v1, v1, v2
	v_accvgpr_read_b32 v2, a17
	v_add_f32_e32 v2, v3, v2
	v_max_f32_e32 v6, 0, v2
	v_accvgpr_read_b32 v2, a18
	v_add_f32_e32 v2, v4, v2
	v_max_f32_e32 v7, 0, v2
	v_accvgpr_read_b32 v2, a19
	v_add_f32_e32 v2, v5, v2
	v_max_f32_e32 v8, 0, v2
	ds_read_b128 v[2:5], v22 offset:53792
	v_max_f32_e32 v1, 0, v1
	s_waitcnt lgkmcnt(0)
	v_add_f32_e32 v2, v9, v2
	v_max_f32_e32 v9, 0, v2
	v_accvgpr_read_b32 v2, a21
	v_add_f32_e32 v2, v3, v2
	v_max_f32_e32 v10, 0, v2
	v_accvgpr_read_b32 v2, a22
	v_add_f32_e32 v2, v4, v2
	v_max_f32_e32 v11, 0, v2
	v_accvgpr_read_b32 v2, a23
	v_add_f32_e32 v2, v5, v2
	v_max_f32_e32 v12, 0, v2
	ds_read_b128 v[2:5], v22 offset:53824
	s_waitcnt lgkmcnt(0)
	v_add_f32_e32 v2, v13, v2
	v_max_f32_e32 v13, 0, v2
	v_accvgpr_read_b32 v2, a25
	v_add_f32_e32 v2, v3, v2
	v_max_f32_e32 v14, 0, v2
	v_accvgpr_read_b32 v2, a26
	v_add_f32_e32 v2, v4, v2
	v_max_f32_e32 v15, 0, v2
	v_accvgpr_read_b32 v2, a27
	v_add_f32_e32 v2, v5, v2
	v_max_f32_e32 v16, 0, v2
	ds_read_b128 v[2:5], v22 offset:53856
	s_waitcnt lgkmcnt(0)
	v_add_f32_e32 v2, v17, v2
	v_max_f32_e32 v17, 0, v2
	v_accvgpr_read_b32 v2, a29
	v_add_f32_e32 v2, v3, v2
	v_max_f32_e32 v18, 0, v2
	v_accvgpr_read_b32 v2, a30
	v_add_f32_e32 v2, v4, v2
	v_max_f32_e32 v19, 0, v2
	v_accvgpr_read_b32 v2, a31
	v_add_f32_e32 v2, v5, v2
	v_max_f32_e32 v20, 0, v2
	v_cvt_pk_f16_f32 v4, v9, v10
	v_cvt_pk_f16_f32 v3, v7, v8
	v_cvt_pk_f16_f32 v2, v1, v6
	ds_read_b128 v[6:9], v0 offset:49152
	v_cvt_pk_f16_f32 v5, v11, v12
	v_accvgpr_read_b32 v1, a0
	s_waitcnt lgkmcnt(0)
	v_mfma_f32_32x32x16_f16 a[32:47], v[6:9], v[2:5], a[32:47]
	ds_read_b128 v[6:9], v0 offset:50176
	v_cvt_pk_f16_f32 v5, v19, v20
	v_cvt_pk_f16_f32 v4, v17, v18
	v_cvt_pk_f16_f32 v3, v15, v16
	v_cvt_pk_f16_f32 v2, v13, v14
	v_accvgpr_read_b32 v13, a8
	v_accvgpr_read_b32 v17, a12
	s_waitcnt lgkmcnt(0)
	v_mfma_f32_32x32x16_f16 a[32:47], v[6:9], v[2:5], a[32:47]
	ds_read_b128 v[2:5], v22 offset:53888
	v_accvgpr_read_b32 v9, a4
	s_waitcnt lgkmcnt(0)
	v_add_f32_e32 v1, v1, v2
	v_accvgpr_read_b32 v2, a1
	v_add_f32_e32 v2, v3, v2
	v_max_f32_e32 v6, 0, v2
	v_accvgpr_read_b32 v2, a2
	v_add_f32_e32 v2, v4, v2
	v_max_f32_e32 v7, 0, v2
	v_accvgpr_read_b32 v2, a3
	v_add_f32_e32 v2, v5, v2
	v_max_f32_e32 v8, 0, v2
	ds_read_b128 v[2:5], v22 offset:53920
	v_max_f32_e32 v1, 0, v1
	s_waitcnt lgkmcnt(0)
	v_add_f32_e32 v2, v9, v2
	v_max_f32_e32 v9, 0, v2
	v_accvgpr_read_b32 v2, a5
	v_add_f32_e32 v2, v3, v2
	v_max_f32_e32 v10, 0, v2
	v_accvgpr_read_b32 v2, a6
	v_add_f32_e32 v2, v4, v2
	v_max_f32_e32 v11, 0, v2
	v_accvgpr_read_b32 v2, a7
	v_add_f32_e32 v2, v5, v2
	v_max_f32_e32 v12, 0, v2
	ds_read_b128 v[2:5], v22 offset:53952
	s_waitcnt lgkmcnt(0)
	v_add_f32_e32 v2, v13, v2
	v_max_f32_e32 v13, 0, v2
	v_accvgpr_read_b32 v2, a9
	v_add_f32_e32 v2, v3, v2
	v_max_f32_e32 v14, 0, v2
	v_accvgpr_read_b32 v2, a10
	v_add_f32_e32 v2, v4, v2
	v_max_f32_e32 v15, 0, v2
	v_accvgpr_read_b32 v2, a11
	v_add_f32_e32 v2, v5, v2
	v_max_f32_e32 v16, 0, v2
	ds_read_b128 v[2:5], v22 offset:53984
	s_waitcnt lgkmcnt(0)
	v_add_f32_e32 v2, v17, v2
	v_max_f32_e32 v17, 0, v2
	v_accvgpr_read_b32 v2, a13
	v_add_f32_e32 v2, v3, v2
	v_max_f32_e32 v18, 0, v2
	v_accvgpr_read_b32 v2, a14
	v_add_f32_e32 v2, v4, v2
	v_max_f32_e32 v19, 0, v2
	v_accvgpr_read_b32 v2, a15
	v_add_f32_e32 v2, v5, v2
	v_max_f32_e32 v20, 0, v2
	v_cvt_pk_f16_f32 v4, v9, v10
	v_cvt_pk_f16_f32 v3, v7, v8
	v_cvt_pk_f16_f32 v2, v1, v6
	ds_read_b128 v[6:9], v0 offset:51200
	v_cvt_pk_f16_f32 v5, v11, v12
	s_waitcnt lgkmcnt(0)
	s_nop 0
	v_mfma_f32_32x32x16_f16 a[32:47], v[6:9], v[2:5], a[32:47]
	ds_read_b128 v[6:9], v0 offset:52224
	v_cvt_pk_f16_f32 v5, v19, v20
	v_cvt_pk_f16_f32 v4, v17, v18
	v_cvt_pk_f16_f32 v3, v15, v16
	v_cvt_pk_f16_f32 v2, v13, v14
	s_waitcnt lgkmcnt(0)
	s_nop 0
	v_mfma_f32_32x32x16_f16 a[32:47], v[6:9], v[2:5], a[32:47]
	s_and_saveexec_b64 s[2:3], s[0:1]
	s_cbranch_execz .LBB3_39
	v_accvgpr_read_b32 v0, a80
	v_accvgpr_read_b32 v6, a86
	v_accvgpr_read_b32 v7, a87
	v_accvgpr_read_b32 v8, a88
	v_accvgpr_read_b32 v9, a89
	v_accvgpr_read_b32 v10, a90
	v_accvgpr_read_b32 v11, a91
	v_accvgpr_read_b32 v12, a92
	v_accvgpr_read_b32 v13, a93
	v_accvgpr_read_b32 v14, a94
	v_accvgpr_read_b32 v15, a95
	v_accvgpr_read_b32 v6, a32
	v_accvgpr_read_b32 v14, a40
	v_accvgpr_read_b32 v15, a41
	v_accvgpr_read_b32 v16, a42
	v_accvgpr_read_b32 v17, a43
	v_accvgpr_read_b32 v18, a44
	v_accvgpr_read_b32 v19, a45
	v_accvgpr_read_b32 v20, a46
	v_accvgpr_read_b32 v21, a47
	ds_read_b128 v[14:17], v22 offset:54016
	ds_read_b128 v[18:21], v22 offset:54080
	v_accvgpr_read_b32 v12, a38
	v_accvgpr_read_b32 v13, a39
	v_lshlrev_b32_e32 v24, 2, v85
	v_accvgpr_read_b32 v1, a81
	v_accvgpr_read_b32 v7, a33
	v_mad_i64_i32 v[12:13], s[0:1], v80, 40, s[18:19]
	v_ashrrev_i32_e32 v25, 31, v24
	v_accvgpr_read_b32 v3, a83
	v_accvgpr_read_b32 v9, a35
	v_lshl_add_u64 v[22:23], v[24:25], 2, v[12:13]
	v_mov_b32_e32 v25, v1
	s_waitcnt lgkmcnt(1)
	v_mov_b32_e32 v27, v15
	v_mov_b32_e32 v1, v7
	s_waitcnt lgkmcnt(0)
	v_mov_b32_e32 v15, v19
	v_accvgpr_read_b32 v2, a82
	v_accvgpr_read_b32 v8, a34
	v_pk_add_f32 v[0:1], v[0:1], v[14:15]
	v_mov_b32_e32 v7, v3
	v_mov_b32_e32 v15, v17
	v_mov_b32_e32 v3, v9
	v_mov_b32_e32 v17, v21
	v_mov_b32_e32 v24, v6
	v_mov_b32_e32 v26, v18
	v_mov_b32_e32 v6, v8
	v_mov_b32_e32 v14, v20
	v_pk_add_f32 v[2:3], v[2:3], v[16:17]
	v_pk_add_f32 v[24:25], v[24:25], v[26:27]
	s_waitcnt vmcnt(0)
	v_pk_mul_f32 v[0:1], v[82:83], v[0:1]
	v_pk_add_f32 v[6:7], v[6:7], v[14:15]
	v_pk_mul_f32 v[2:3], v[82:83], v[2:3]
	v_accvgpr_read_b32 v4, a84
	v_accvgpr_read_b32 v5, a85
	v_accvgpr_read_b32 v10, a36
	v_accvgpr_read_b32 v11, a37
	v_pk_fma_f32 v[0:1], v[82:83], v[24:25], v[0:1] op_sel:[1,0,0] op_sel_hi:[0,1,1]
	v_pk_fma_f32 v[2:3], v[82:83], v[6:7], v[2:3] op_sel:[1,0,0] op_sel_hi:[0,1,1]
	v_cmp_eq_u32_e32 vcc, 0, v85
	global_store_dwordx4 v[22:23], v[0:3], off
	s_and_b64 exec, exec, vcc
	s_cbranch_execz .LBB3_39
	s_mov_b32 s0, 0xd000
	v_add_u32_e64 v0, s0, 0
	ds_read2_b64 v[0:3], v0 offset0:100 offset1:108
	v_mov_b32_e32 v9, v5
	v_mov_b32_e32 v5, v11
	v_mov_b32_e32 v8, v10
	v_pk_mov_b32 v[6:7], v[82:83], v[82:83] op_sel:[1,0]
	s_waitcnt lgkmcnt(0)
	v_mov_b32_e32 v15, v1
	v_mov_b32_e32 v1, v3
	v_mov_b32_e32 v14, v2
	v_pk_add_f32 v[0:1], v[4:5], v[0:1]
	v_pk_add_f32 v[8:9], v[8:9], v[14:15]
	v_pk_mul_f32 v[0:1], v[82:83], v[0:1]
	s_nop 0
	v_pk_fma_f32 v[0:1], v[6:7], v[8:9], v[0:1]
	global_store_dwordx2 v[12:13], v[0:1], off offset:32
